# v28 + saddr LDS-DMA form in the K-loops of P1 P2 P5 P7 P8a P8b P10 (and 2 pieces each in P14 P16)
# baseline (speedup 1.0000x reference)
.LBB0_103:
	ds_read_b128 v[154:157], v151
	ds_read_b128 v[158:161], v151 offset:1024
	ds_read_b128 v[162:165], v151 offset:2048
	ds_read_b128 v[166:169], v151 offset:3072
	ds_read_b128 v[170:173], v152
	ds_read_b128 v[174:177], v152 offset:1024
	ds_read_b128 v[178:181], v152 offset:2048
	ds_read_b128 v[182:185], v152 offset:3072
	s_add_i32 m0, s39, 0xc000
	ds_read_b128 v[186:189], v153
	ds_read_b128 v[190:193], v153 offset:1024
	ds_read_b128 v[194:197], v153 offset:2048
	ds_read_b128 v[198:201], v153 offset:3072
	ds_read_b128 v[202:205], v153 offset:4096
	ds_read_b128 v[206:209], v153 offset:5120
	ds_read_b128 v[210:213], v153 offset:6144
	ds_read_b128 v[214:217], v153 offset:7168
	global_load_lds_dwordx4 v[144:145], off
	s_add_i32 m0, s39, 0xe000
	s_nop 0
	global_load_lds_dwordx4 v[146:147], off
	s_waitcnt vmcnt(8)
	s_waitcnt lgkmcnt(0)
	s_barrier
	s_setprio 1
	s_waitcnt lgkmcnt(0)
	v_mfma_f32_16x16x32_bf16 v[124:127], v[154:157], v[186:189], v[124:127]
	v_mfma_f32_16x16x32_bf16 v[120:123], v[162:165], v[186:189], v[120:123]
	v_mfma_f32_16x16x32_bf16 v[108:111], v[154:157], v[194:197], v[108:111]
	v_mfma_f32_16x16x32_bf16 v[104:107], v[162:165], v[194:197], v[104:107]
	v_mfma_f32_16x16x32_bf16 v[92:95], v[154:157], v[202:205], v[92:95]
	v_mfma_f32_16x16x32_bf16 v[88:91], v[162:165], v[202:205], v[88:91]
	v_mfma_f32_16x16x32_bf16 v[76:79], v[154:157], v[210:213], v[76:79]
	v_mfma_f32_16x16x32_bf16 v[72:75], v[162:165], v[210:213], v[72:75]
	v_mfma_f32_16x16x32_bf16 v[124:127], v[158:161], v[190:193], v[124:127]
	v_mfma_f32_16x16x32_bf16 v[120:123], v[166:169], v[190:193], v[120:123]
	v_mfma_f32_16x16x32_bf16 v[108:111], v[158:161], v[198:201], v[108:111]
	v_mfma_f32_16x16x32_bf16 v[104:107], v[166:169], v[198:201], v[104:107]
	v_mfma_f32_16x16x32_bf16 v[92:95], v[158:161], v[206:209], v[92:95]
	v_mfma_f32_16x16x32_bf16 v[88:91], v[166:169], v[206:209], v[88:91]
	v_mfma_f32_16x16x32_bf16 v[76:79], v[158:161], v[214:217], v[76:79]
	v_mfma_f32_16x16x32_bf16 v[72:75], v[166:169], v[214:217], v[72:75]
	s_setprio 0
	s_setprio 1
	v_mfma_f32_16x16x32_bf16 v[116:119], v[170:173], v[186:189], v[116:119]
	v_mfma_f32_16x16x32_bf16 v[112:115], v[178:181], v[186:189], v[112:115]
	v_mfma_f32_16x16x32_bf16 v[100:103], v[170:173], v[194:197], v[100:103]
	v_mfma_f32_16x16x32_bf16 v[96:99], v[178:181], v[194:197], v[96:99]
	v_mfma_f32_16x16x32_bf16 v[84:87], v[170:173], v[202:205], v[84:87]
	v_mfma_f32_16x16x32_bf16 v[80:83], v[178:181], v[202:205], v[80:83]
	v_mfma_f32_16x16x32_bf16 v[68:71], v[170:173], v[210:213], v[68:71]
	v_mfma_f32_16x16x32_bf16 v[64:67], v[178:181], v[210:213], v[64:67]
	v_mfma_f32_16x16x32_bf16 v[116:119], v[174:177], v[190:193], v[116:119]
	v_mfma_f32_16x16x32_bf16 v[112:115], v[182:185], v[190:193], v[112:115]
	v_mfma_f32_16x16x32_bf16 v[100:103], v[174:177], v[198:201], v[100:103]
	v_mfma_f32_16x16x32_bf16 v[96:99], v[182:185], v[198:201], v[96:99]
	v_mfma_f32_16x16x32_bf16 v[84:87], v[174:177], v[206:209], v[84:87]
	v_mfma_f32_16x16x32_bf16 v[80:83], v[182:185], v[206:209], v[80:83]
	v_mfma_f32_16x16x32_bf16 v[68:71], v[174:177], v[214:217], v[68:71]
	v_mfma_f32_16x16x32_bf16 v[64:67], v[182:185], v[214:217], v[64:67]
	s_setprio 0
	s_barrier
	s_cmp_gt_u32 s11, 13
	s_cselect_b64 s[90:91], -1, 0
	s_and_b64 s[36:37], s[90:91], exec
	v_sub_co_u32_e64 v218, s[36:37], s11, 14
	s_nop 0
	v_readfirstlane_b32 s94, v218
	s_cselect_b32 s29, s35, s57
	s_cselect_b32 s89, s34, s56
	s_add_i32 s95, s94, 16
	s_and_b64 s[92:93], s[90:91], exec
	s_cselect_b32 s92, s94, s95
	s_ashr_i32 s93, s92, 31
	s_lshl_b64 s[92:93], s[92:93], 7
	s_add_u32 s94, s89, s92
	s_addc_u32 s95, s29, s93
	s_add_i32 s29, s86, s78
	s_mov_b32 m0, s29
	ds_read_b128 v[186:189], v153 offset:16384
	ds_read_b128 v[190:193], v153 offset:17408
	ds_read_b128 v[194:197], v153 offset:18432
	ds_read_b128 v[198:201], v153 offset:19456
	ds_read_b128 v[202:205], v153 offset:20480
	ds_read_b128 v[206:209], v153 offset:21504
	ds_read_b128 v[210:213], v153 offset:22528
	ds_read_b128 v[214:217], v153 offset:23552
	global_load_lds_dwordx4 v130, s[94:95]
	s_add_i32 m0, s29, 0x2000
	s_add_i32 s29, s87, s78
	global_load_lds_dwordx4 v134, s[94:95]
	s_add_u32 s94, s94, 0x40000
	s_addc_u32 s95, s95, 0
	s_mov_b32 m0, s29
	s_nop 0
	global_load_lds_dwordx4 v130, s[94:95]
	s_add_i32 m0, s29, 0x2000
	s_and_b64 s[90:91], s[90:91], exec
	s_cselect_b32 s89, s30, s60
	s_cselect_b32 s29, s31, s61
	s_add_u32 s90, s89, s92
	s_addc_u32 s91, s29, s93
	global_load_lds_dwordx4 v134, s[94:95]
	s_mov_b32 m0, s39
	s_nop 0
	global_load_lds_dwordx4 v128, s[90:91]
	s_mov_b32 m0, s79
	s_nop 0
	global_load_lds_dwordx4 v132, s[90:91]
	s_waitcnt vmcnt(8)
	s_waitcnt lgkmcnt(0)
	s_barrier
	s_setprio 1
	s_waitcnt lgkmcnt(0)
	v_mfma_f32_16x16x32_bf16 v[60:63], v[154:157], v[186:189], v[60:63]
	v_mfma_f32_16x16x32_bf16 v[56:59], v[162:165], v[186:189], v[56:59]
	v_mfma_f32_16x16x32_bf16 v[44:47], v[154:157], v[194:197], v[44:47]
	v_mfma_f32_16x16x32_bf16 v[40:43], v[162:165], v[194:197], v[40:43]
	v_mfma_f32_16x16x32_bf16 v[20:23], v[154:157], v[202:205], v[20:23]
	v_mfma_f32_16x16x32_bf16 v[16:19], v[162:165], v[202:205], v[16:19]
	v_mfma_f32_16x16x32_bf16 v[4:7], v[154:157], v[210:213], v[4:7]
	v_mfma_f32_16x16x32_bf16 v[0:3], v[162:165], v[210:213], v[0:3]
	v_mfma_f32_16x16x32_bf16 v[60:63], v[158:161], v[190:193], v[60:63]
	v_mfma_f32_16x16x32_bf16 v[56:59], v[166:169], v[190:193], v[56:59]
	v_mfma_f32_16x16x32_bf16 v[44:47], v[158:161], v[198:201], v[44:47]
	v_mfma_f32_16x16x32_bf16 v[40:43], v[166:169], v[198:201], v[40:43]
	v_mfma_f32_16x16x32_bf16 v[20:23], v[158:161], v[206:209], v[20:23]
	v_mfma_f32_16x16x32_bf16 v[16:19], v[166:169], v[206:209], v[16:19]
	v_mfma_f32_16x16x32_bf16 v[4:7], v[158:161], v[214:217], v[4:7]
	v_mfma_f32_16x16x32_bf16 v[0:3], v[166:169], v[214:217], v[0:3]
	s_setprio 0
	s_setprio 1
	v_mfma_f32_16x16x32_bf16 v[52:55], v[170:173], v[186:189], v[52:55]
	v_mfma_f32_16x16x32_bf16 v[48:51], v[178:181], v[186:189], v[48:51]
	v_mfma_f32_16x16x32_bf16 v[36:39], v[170:173], v[194:197], v[36:39]
	v_mfma_f32_16x16x32_bf16 v[32:35], v[178:181], v[194:197], v[32:35]
	v_mfma_f32_16x16x32_bf16 v[28:31], v[170:173], v[202:205], v[28:31]
	v_mfma_f32_16x16x32_bf16 v[24:27], v[178:181], v[202:205], v[24:27]
	v_mfma_f32_16x16x32_bf16 v[12:15], v[170:173], v[210:213], v[12:15]
	v_mfma_f32_16x16x32_bf16 v[8:11], v[178:181], v[210:213], v[8:11]
	v_mfma_f32_16x16x32_bf16 v[52:55], v[174:177], v[190:193], v[52:55]
	v_mfma_f32_16x16x32_bf16 v[48:51], v[182:185], v[190:193], v[48:51]
	v_mfma_f32_16x16x32_bf16 v[36:39], v[174:177], v[198:201], v[36:39]
	v_mfma_f32_16x16x32_bf16 v[32:35], v[182:185], v[198:201], v[32:35]
	v_mfma_f32_16x16x32_bf16 v[28:31], v[174:177], v[206:209], v[28:31]
	v_mfma_f32_16x16x32_bf16 v[24:27], v[182:185], v[206:209], v[24:27]
	v_mfma_f32_16x16x32_bf16 v[12:15], v[174:177], v[214:217], v[12:15]
	v_mfma_f32_16x16x32_bf16 v[8:11], v[182:185], v[214:217], v[8:11]
	s_setprio 0
	s_barrier
	s_add_i32 s29, 0, 0x18000
	s_add_i32 s89, 0, 0x1c000
	v_add_u32_e32 v166, s29, v149
	v_add_u32_e32 v182, s89, v149
	ds_read_b128 v[154:157], v166
	ds_read_b128 v[158:161], v166 offset:1024
	ds_read_b128 v[162:165], v166 offset:2048
	ds_read_b128 v[166:169], v166 offset:3072
	ds_read_b128 v[170:173], v182
	ds_read_b128 v[174:177], v182 offset:1024
	ds_read_b128 v[178:181], v182 offset:2048
	ds_read_b128 v[182:185], v182 offset:3072
	s_add_u32 s90, s90, 0x40000
	s_addc_u32 s91, s91, 0
	s_mov_b32 m0, s80
	ds_read_b128 v[186:189], v153 offset:32768
	ds_read_b128 v[190:193], v153 offset:33792
	ds_read_b128 v[194:197], v153 offset:34816
	ds_read_b128 v[198:201], v153 offset:35840
	ds_read_b128 v[202:205], v153 offset:36864
	ds_read_b128 v[206:209], v153 offset:37888
	ds_read_b128 v[210:213], v153 offset:38912
	ds_read_b128 v[214:217], v153 offset:39936
	global_load_lds_dwordx4 v128, s[90:91]
	s_mov_b32 m0, s81
	s_nop 0
	global_load_lds_dwordx4 v132, s[90:91]
	s_waitcnt vmcnt(8)
	s_waitcnt lgkmcnt(0)
	s_barrier
	s_setprio 1
	s_waitcnt lgkmcnt(0)
	v_mfma_f32_16x16x32_bf16 v[124:127], v[154:157], v[186:189], v[124:127]
	v_mfma_f32_16x16x32_bf16 v[120:123], v[162:165], v[186:189], v[120:123]
	v_mfma_f32_16x16x32_bf16 v[108:111], v[154:157], v[194:197], v[108:111]
	v_mfma_f32_16x16x32_bf16 v[104:107], v[162:165], v[194:197], v[104:107]
	v_mfma_f32_16x16x32_bf16 v[92:95], v[154:157], v[202:205], v[92:95]
	v_mfma_f32_16x16x32_bf16 v[88:91], v[162:165], v[202:205], v[88:91]
	v_mfma_f32_16x16x32_bf16 v[76:79], v[154:157], v[210:213], v[76:79]
	v_mfma_f32_16x16x32_bf16 v[72:75], v[162:165], v[210:213], v[72:75]
	v_mfma_f32_16x16x32_bf16 v[124:127], v[158:161], v[190:193], v[124:127]
	v_mfma_f32_16x16x32_bf16 v[120:123], v[166:169], v[190:193], v[120:123]
	v_mfma_f32_16x16x32_bf16 v[108:111], v[158:161], v[198:201], v[108:111]
	v_mfma_f32_16x16x32_bf16 v[104:107], v[166:169], v[198:201], v[104:107]
	v_mfma_f32_16x16x32_bf16 v[92:95], v[158:161], v[206:209], v[92:95]
	v_mfma_f32_16x16x32_bf16 v[88:91], v[166:169], v[206:209], v[88:91]
	v_mfma_f32_16x16x32_bf16 v[76:79], v[158:161], v[214:217], v[76:79]
	v_mfma_f32_16x16x32_bf16 v[72:75], v[166:169], v[214:217], v[72:75]
	s_setprio 0
	s_setprio 1
	v_mfma_f32_16x16x32_bf16 v[116:119], v[170:173], v[186:189], v[116:119]
	v_mfma_f32_16x16x32_bf16 v[112:115], v[178:181], v[186:189], v[112:115]
	v_mfma_f32_16x16x32_bf16 v[100:103], v[170:173], v[194:197], v[100:103]
	v_mfma_f32_16x16x32_bf16 v[96:99], v[178:181], v[194:197], v[96:99]
	v_mfma_f32_16x16x32_bf16 v[84:87], v[170:173], v[202:205], v[84:87]
	v_mfma_f32_16x16x32_bf16 v[80:83], v[178:181], v[202:205], v[80:83]
	v_mfma_f32_16x16x32_bf16 v[68:71], v[170:173], v[210:213], v[68:71]
	v_mfma_f32_16x16x32_bf16 v[64:67], v[178:181], v[210:213], v[64:67]
	v_mfma_f32_16x16x32_bf16 v[116:119], v[174:177], v[190:193], v[116:119]
	v_mfma_f32_16x16x32_bf16 v[112:115], v[182:185], v[190:193], v[112:115]
	v_mfma_f32_16x16x32_bf16 v[100:103], v[174:177], v[198:201], v[100:103]
	v_mfma_f32_16x16x32_bf16 v[96:99], v[182:185], v[198:201], v[96:99]
	v_mfma_f32_16x16x32_bf16 v[84:87], v[174:177], v[206:209], v[84:87]
	v_mfma_f32_16x16x32_bf16 v[80:83], v[182:185], v[206:209], v[80:83]
	v_mfma_f32_16x16x32_bf16 v[68:71], v[174:177], v[214:217], v[68:71]
	v_mfma_f32_16x16x32_bf16 v[64:67], v[182:185], v[214:217], v[64:67]
	s_setprio 0
	s_barrier
	s_cmp_gt_u32 s11, 12
	s_cselect_b64 s[90:91], -1, 0
	s_and_b64 s[92:93], s[90:91], exec
	s_cselect_b32 s92, -13, 3
	s_cselect_b32 s95, s35, s57
	s_cselect_b32 s94, s34, s56
	s_add_i32 s92, s92, s11
	s_ashr_i32 s93, s92, 31
	s_lshl_b64 s[92:93], s[92:93], 7
	s_add_u32 s94, s94, s92
	s_addc_u32 s95, s95, s93
	s_add_i32 s29, s29, s78
	s_mov_b32 m0, s29
	ds_read_b128 v[186:189], v153 offset:49152
	ds_read_b128 v[190:193], v153 offset:50176
	ds_read_b128 v[194:197], v153 offset:51200
	ds_read_b128 v[198:201], v153 offset:52224
	ds_read_b128 v[202:205], v153 offset:53248
	ds_read_b128 v[206:209], v153 offset:54272
	ds_read_b128 v[210:213], v153 offset:55296
	ds_read_b128 v[214:217], v153 offset:56320
	global_load_lds_dwordx4 v130, s[94:95]
	s_add_i32 m0, s29, 0x2000
	s_add_i32 s29, s89, s78
	global_load_lds_dwordx4 v134, s[94:95]
	s_add_u32 s94, s94, 0x40000
	s_addc_u32 s95, s95, 0
	s_mov_b32 m0, s29
	s_nop 0
	global_load_lds_dwordx4 v130, s[94:95]
	s_add_i32 m0, s29, 0x2000
	s_and_b64 s[90:91], s[90:91], exec
	s_cselect_b32 s89, s30, s60
	s_cselect_b32 s29, s31, s61
	s_add_u32 s90, s89, s92
	s_addc_u32 s91, s29, s93
	global_load_lds_dwordx4 v134, s[94:95]
	s_mov_b32 m0, s83
	s_nop 0
	global_load_lds_dwordx4 v128, s[90:91]
	s_mov_b32 m0, s84
	s_nop 0
	global_load_lds_dwordx4 v132, s[90:91]
	s_waitcnt vmcnt(8)
	s_waitcnt lgkmcnt(0)
	s_barrier
	s_setprio 1
	s_waitcnt lgkmcnt(0)
	v_mfma_f32_16x16x32_bf16 v[60:63], v[154:157], v[186:189], v[60:63]
	v_mfma_f32_16x16x32_bf16 v[56:59], v[162:165], v[186:189], v[56:59]
	v_mfma_f32_16x16x32_bf16 v[44:47], v[154:157], v[194:197], v[44:47]
	v_mfma_f32_16x16x32_bf16 v[40:43], v[162:165], v[194:197], v[40:43]
	v_mfma_f32_16x16x32_bf16 v[20:23], v[154:157], v[202:205], v[20:23]
	v_mfma_f32_16x16x32_bf16 v[16:19], v[162:165], v[202:205], v[16:19]
	v_mfma_f32_16x16x32_bf16 v[4:7], v[154:157], v[210:213], v[4:7]
	v_mfma_f32_16x16x32_bf16 v[0:3], v[162:165], v[210:213], v[0:3]
	v_mfma_f32_16x16x32_bf16 v[60:63], v[158:161], v[190:193], v[60:63]
	v_mfma_f32_16x16x32_bf16 v[56:59], v[166:169], v[190:193], v[56:59]
	v_mfma_f32_16x16x32_bf16 v[44:47], v[158:161], v[198:201], v[44:47]
	v_mfma_f32_16x16x32_bf16 v[40:43], v[166:169], v[198:201], v[40:43]
	v_mfma_f32_16x16x32_bf16 v[20:23], v[158:161], v[206:209], v[20:23]
	v_mfma_f32_16x16x32_bf16 v[16:19], v[166:169], v[206:209], v[16:19]
	v_mfma_f32_16x16x32_bf16 v[4:7], v[158:161], v[214:217], v[4:7]
	v_mfma_f32_16x16x32_bf16 v[0:3], v[166:169], v[214:217], v[0:3]
	s_setprio 0
	s_setprio 1
	v_mfma_f32_16x16x32_bf16 v[52:55], v[170:173], v[186:189], v[52:55]
	v_mfma_f32_16x16x32_bf16 v[48:51], v[178:181], v[186:189], v[48:51]
	v_mfma_f32_16x16x32_bf16 v[36:39], v[170:173], v[194:197], v[36:39]
	v_mfma_f32_16x16x32_bf16 v[32:35], v[178:181], v[194:197], v[32:35]
	v_mfma_f32_16x16x32_bf16 v[28:31], v[170:173], v[202:205], v[28:31]
	v_mfma_f32_16x16x32_bf16 v[24:27], v[178:181], v[202:205], v[24:27]
	v_mfma_f32_16x16x32_bf16 v[12:15], v[170:173], v[210:213], v[12:15]
	v_mfma_f32_16x16x32_bf16 v[8:11], v[178:181], v[210:213], v[8:11]
	v_mfma_f32_16x16x32_bf16 v[52:55], v[174:177], v[190:193], v[52:55]
	v_mfma_f32_16x16x32_bf16 v[48:51], v[182:185], v[190:193], v[48:51]
	v_mfma_f32_16x16x32_bf16 v[36:39], v[174:177], v[198:201], v[36:39]
	v_mfma_f32_16x16x32_bf16 v[32:35], v[182:185], v[198:201], v[32:35]
	v_mfma_f32_16x16x32_bf16 v[28:31], v[174:177], v[206:209], v[28:31]
	v_mfma_f32_16x16x32_bf16 v[24:27], v[182:185], v[206:209], v[24:27]
	v_mfma_f32_16x16x32_bf16 v[12:15], v[174:177], v[214:217], v[12:15]
	v_mfma_f32_16x16x32_bf16 v[8:11], v[182:185], v[214:217], v[8:11]
	s_setprio 0
	s_barrier
	v_lshl_add_u64 v[144:145], v[144:145], 0, s[8:9]
	v_lshl_add_u64 v[146:147], v[146:147], 0, s[8:9]
	s_add_i32 s11, s11, 2
	s_and_b64 vcc, exec, s[36:37]
	s_cbranch_vccnz .LBB0_103
	s_andn2_b64 vcc, exec, s[6:7]
	s_cbranch_vccnz .LBB0_106
	s_barrier

.LBB0_124:
	ds_read_b128 v[152:155], v164
	ds_read_b128 v[156:159], v164 offset:1024
	ds_read_b128 v[168:171], v164 offset:2048
	ds_read_b128 v[172:175], v164 offset:3072
	ds_read_b128 v[176:179], v165
	ds_read_b128 v[180:183], v165 offset:1024
	ds_read_b128 v[184:187], v165 offset:2048
	ds_read_b128 v[188:191], v165 offset:3072
	s_add_i32 m0, s79, 0xc000
	ds_read_b128 v[192:195], v166
	ds_read_b128 v[196:199], v166 offset:1024
	ds_read_b128 v[200:203], v166 offset:2048
	ds_read_b128 v[204:207], v166 offset:3072
	ds_read_b128 v[208:211], v166 offset:4096
	ds_read_b128 v[212:215], v166 offset:5120
	ds_read_b128 v[216:219], v166 offset:6144
	ds_read_b128 v[220:223], v166 offset:7168
	global_load_lds_dwordx4 v[128:129], off
	s_add_i32 m0, s79, 0xe000
	s_nop 0
	global_load_lds_dwordx4 v[130:131], off
	s_waitcnt vmcnt(8)
	s_waitcnt lgkmcnt(0)
	s_barrier
	s_setprio 1
	s_waitcnt lgkmcnt(0)
	v_mfma_f32_16x16x32_bf16 v[124:127], v[152:155], v[192:195], v[124:127]
	v_mfma_f32_16x16x32_bf16 v[120:123], v[168:171], v[192:195], v[120:123]
	v_mfma_f32_16x16x32_bf16 v[108:111], v[152:155], v[200:203], v[108:111]
	v_mfma_f32_16x16x32_bf16 v[104:107], v[168:171], v[200:203], v[104:107]
	v_mfma_f32_16x16x32_bf16 v[92:95], v[152:155], v[208:211], v[92:95]
	v_mfma_f32_16x16x32_bf16 v[88:91], v[168:171], v[208:211], v[88:91]
	v_mfma_f32_16x16x32_bf16 v[76:79], v[152:155], v[216:219], v[76:79]
	v_mfma_f32_16x16x32_bf16 v[72:75], v[168:171], v[216:219], v[72:75]
	v_mfma_f32_16x16x32_bf16 v[124:127], v[156:159], v[196:199], v[124:127]
	v_mfma_f32_16x16x32_bf16 v[120:123], v[172:175], v[196:199], v[120:123]
	v_mfma_f32_16x16x32_bf16 v[108:111], v[156:159], v[204:207], v[108:111]
	v_mfma_f32_16x16x32_bf16 v[104:107], v[172:175], v[204:207], v[104:107]
	v_mfma_f32_16x16x32_bf16 v[92:95], v[156:159], v[212:215], v[92:95]
	v_mfma_f32_16x16x32_bf16 v[88:91], v[172:175], v[212:215], v[88:91]
	v_mfma_f32_16x16x32_bf16 v[76:79], v[156:159], v[220:223], v[76:79]
	v_mfma_f32_16x16x32_bf16 v[72:75], v[172:175], v[220:223], v[72:75]
	s_setprio 0
	s_setprio 1
	v_mfma_f32_16x16x32_bf16 v[116:119], v[176:179], v[192:195], v[116:119]
	v_mfma_f32_16x16x32_bf16 v[112:115], v[184:187], v[192:195], v[112:115]
	v_mfma_f32_16x16x32_bf16 v[100:103], v[176:179], v[200:203], v[100:103]
	v_mfma_f32_16x16x32_bf16 v[96:99], v[184:187], v[200:203], v[96:99]
	v_mfma_f32_16x16x32_bf16 v[84:87], v[176:179], v[208:211], v[84:87]
	v_mfma_f32_16x16x32_bf16 v[80:83], v[184:187], v[208:211], v[80:83]
	v_mfma_f32_16x16x32_bf16 v[68:71], v[176:179], v[216:219], v[68:71]
	v_mfma_f32_16x16x32_bf16 v[64:67], v[184:187], v[216:219], v[64:67]
	v_mfma_f32_16x16x32_bf16 v[116:119], v[180:183], v[196:199], v[116:119]
	v_mfma_f32_16x16x32_bf16 v[112:115], v[188:191], v[196:199], v[112:115]
	v_mfma_f32_16x16x32_bf16 v[100:103], v[180:183], v[204:207], v[100:103]
	v_mfma_f32_16x16x32_bf16 v[96:99], v[188:191], v[204:207], v[96:99]
	v_mfma_f32_16x16x32_bf16 v[84:87], v[180:183], v[212:215], v[84:87]
	v_mfma_f32_16x16x32_bf16 v[80:83], v[188:191], v[212:215], v[80:83]
	v_mfma_f32_16x16x32_bf16 v[68:71], v[180:183], v[220:223], v[68:71]
	v_mfma_f32_16x16x32_bf16 v[64:67], v[188:191], v[220:223], v[64:67]
	s_setprio 0
	s_barrier
	s_cmp_gt_u32 s0, 13
	s_cselect_b64 vcc, -1, 0
	s_and_b64 s[36:37], vcc, exec
	v_sub_co_u32_e64 v160, s[36:37], s0, 14
	s_nop 0
	v_readfirstlane_b32 s39, v160
	s_cselect_b32 s7, s75, s83
	s_cselect_b32 s6, s74, s82
	s_add_i32 s57, s39, 16
	s_and_b64 s[34:35], vcc, exec
	s_cselect_b32 s34, s39, s57
	s_ashr_i32 s35, s34, 31
	s_lshl_b64 s[34:35], s[34:35], 7
	s_add_u32 s6, s6, s34
	s_addc_u32 s7, s7, s35
	s_add_i32 s39, s76, s29
	s_mov_b32 m0, s39
	ds_read_b128 v[192:195], v166 offset:16384
	ds_read_b128 v[196:199], v166 offset:17408
	ds_read_b128 v[200:203], v166 offset:18432
	ds_read_b128 v[204:207], v166 offset:19456
	ds_read_b128 v[208:211], v166 offset:20480
	ds_read_b128 v[212:215], v166 offset:21504
	ds_read_b128 v[216:219], v166 offset:22528
	ds_read_b128 v[220:223], v166 offset:23552
	global_load_lds_dwordx4 v134, s[6:7]
	s_add_i32 m0, s39, 0x2000
	s_add_i32 s39, s4, s29
	global_load_lds_dwordx4 v138, s[6:7]
	s_add_u32 s6, s6, 0x40000
	s_addc_u32 s7, s7, 0
	s_mov_b32 m0, s39
	s_nop 0
	global_load_lds_dwordx4 v134, s[6:7]
	s_add_i32 m0, s39, 0x2000
	v_lshl_add_u64 v[160:161], s[6:7], 0, v[138:139]
	s_and_b64 s[6:7], vcc, exec
	s_cselect_b32 s6, s60, s80
	s_cselect_b32 s7, s61, s81
	s_add_u32 s6, s6, s34
	s_addc_u32 s7, s7, s35
	global_load_lds_dwordx4 v[160:161], off
	s_mov_b32 m0, s79
	s_nop 0
	global_load_lds_dwordx4 v132, s[6:7]
	s_mov_b32 m0, s87
	s_nop 0
	global_load_lds_dwordx4 v136, s[6:7]
	s_waitcnt vmcnt(8)
	s_waitcnt lgkmcnt(0)
	s_barrier
	s_setprio 1
	s_waitcnt lgkmcnt(0)
	v_mfma_f32_16x16x32_bf16 v[60:63], v[152:155], v[192:195], v[60:63]
	v_mfma_f32_16x16x32_bf16 v[56:59], v[168:171], v[192:195], v[56:59]
	v_mfma_f32_16x16x32_bf16 v[44:47], v[152:155], v[200:203], v[44:47]
	v_mfma_f32_16x16x32_bf16 v[40:43], v[168:171], v[200:203], v[40:43]
	v_mfma_f32_16x16x32_bf16 v[28:31], v[152:155], v[208:211], v[28:31]
	v_mfma_f32_16x16x32_bf16 v[16:19], v[168:171], v[208:211], v[16:19]
	v_mfma_f32_16x16x32_bf16 v[8:11], v[152:155], v[216:219], v[8:11]
	v_mfma_f32_16x16x32_bf16 v[0:3], v[168:171], v[216:219], v[0:3]
	v_mfma_f32_16x16x32_bf16 v[60:63], v[156:159], v[196:199], v[60:63]
	v_mfma_f32_16x16x32_bf16 v[56:59], v[172:175], v[196:199], v[56:59]
	v_mfma_f32_16x16x32_bf16 v[44:47], v[156:159], v[204:207], v[44:47]
	v_mfma_f32_16x16x32_bf16 v[40:43], v[172:175], v[204:207], v[40:43]
	v_mfma_f32_16x16x32_bf16 v[28:31], v[156:159], v[212:215], v[28:31]
	v_mfma_f32_16x16x32_bf16 v[16:19], v[172:175], v[212:215], v[16:19]
	v_mfma_f32_16x16x32_bf16 v[8:11], v[156:159], v[220:223], v[8:11]
	v_mfma_f32_16x16x32_bf16 v[0:3], v[172:175], v[220:223], v[0:3]
	s_setprio 0
	s_setprio 1
	v_mfma_f32_16x16x32_bf16 v[52:55], v[176:179], v[192:195], v[52:55]
	v_mfma_f32_16x16x32_bf16 v[48:51], v[184:187], v[192:195], v[48:51]
	v_mfma_f32_16x16x32_bf16 v[36:39], v[176:179], v[200:203], v[36:39]
	v_mfma_f32_16x16x32_bf16 v[32:35], v[184:187], v[200:203], v[32:35]
	v_mfma_f32_16x16x32_bf16 v[24:27], v[176:179], v[208:211], v[24:27]
	v_mfma_f32_16x16x32_bf16 v[20:23], v[184:187], v[208:211], v[20:23]
	v_mfma_f32_16x16x32_bf16 v[12:15], v[176:179], v[216:219], v[12:15]
	v_mfma_f32_16x16x32_bf16 v[4:7], v[184:187], v[216:219], v[4:7]
	v_mfma_f32_16x16x32_bf16 v[52:55], v[180:183], v[196:199], v[52:55]
	v_mfma_f32_16x16x32_bf16 v[48:51], v[188:191], v[196:199], v[48:51]
	v_mfma_f32_16x16x32_bf16 v[36:39], v[180:183], v[204:207], v[36:39]
	v_mfma_f32_16x16x32_bf16 v[32:35], v[188:191], v[204:207], v[32:35]
	v_mfma_f32_16x16x32_bf16 v[24:27], v[180:183], v[212:215], v[24:27]
	v_mfma_f32_16x16x32_bf16 v[20:23], v[188:191], v[212:215], v[20:23]
	v_mfma_f32_16x16x32_bf16 v[12:15], v[180:183], v[220:223], v[12:15]
	v_mfma_f32_16x16x32_bf16 v[4:7], v[188:191], v[220:223], v[4:7]
	s_setprio 0
	s_barrier
	s_add_i32 s39, 0, 0x18000
	v_add_u32_e32 v160, s39, v162
	s_add_i32 s57, 0, 0x1c000
	ds_read_b128 v[152:155], v160
	ds_read_b128 v[156:159], v160 offset:1024
	ds_read_b128 v[168:171], v160 offset:2048
	ds_read_b128 v[172:175], v160 offset:3072
	v_add_u32_e32 v160, s57, v162
	ds_read_b128 v[176:179], v160
	ds_read_b128 v[180:183], v160 offset:1024
	ds_read_b128 v[184:187], v160 offset:2048
	ds_read_b128 v[188:191], v160 offset:3072
	s_add_u32 s6, s6, 0x40000
	s_addc_u32 s7, s7, 0
	s_mov_b32 m0, s88
	ds_read_b128 v[192:195], v166 offset:32768
	ds_read_b128 v[196:199], v166 offset:33792
	ds_read_b128 v[200:203], v166 offset:34816
	ds_read_b128 v[204:207], v166 offset:35840
	ds_read_b128 v[208:211], v166 offset:36864
	ds_read_b128 v[212:215], v166 offset:37888
	ds_read_b128 v[216:219], v166 offset:38912
	ds_read_b128 v[220:223], v166 offset:39936
	global_load_lds_dwordx4 v132, s[6:7]
	s_mov_b32 m0, s89
	s_nop 0
	global_load_lds_dwordx4 v136, s[6:7]
	s_waitcnt vmcnt(8)
	s_waitcnt lgkmcnt(0)
	s_barrier
	s_setprio 1
	s_waitcnt lgkmcnt(0)
	v_mfma_f32_16x16x32_bf16 v[124:127], v[152:155], v[192:195], v[124:127]
	v_mfma_f32_16x16x32_bf16 v[120:123], v[168:171], v[192:195], v[120:123]
	v_mfma_f32_16x16x32_bf16 v[108:111], v[152:155], v[200:203], v[108:111]
	v_mfma_f32_16x16x32_bf16 v[104:107], v[168:171], v[200:203], v[104:107]
	v_mfma_f32_16x16x32_bf16 v[92:95], v[152:155], v[208:211], v[92:95]
	v_mfma_f32_16x16x32_bf16 v[88:91], v[168:171], v[208:211], v[88:91]
	v_mfma_f32_16x16x32_bf16 v[76:79], v[152:155], v[216:219], v[76:79]
	v_mfma_f32_16x16x32_bf16 v[72:75], v[168:171], v[216:219], v[72:75]
	v_mfma_f32_16x16x32_bf16 v[124:127], v[156:159], v[196:199], v[124:127]
	v_mfma_f32_16x16x32_bf16 v[120:123], v[172:175], v[196:199], v[120:123]
	v_mfma_f32_16x16x32_bf16 v[108:111], v[156:159], v[204:207], v[108:111]
	v_mfma_f32_16x16x32_bf16 v[104:107], v[172:175], v[204:207], v[104:107]
	v_mfma_f32_16x16x32_bf16 v[92:95], v[156:159], v[212:215], v[92:95]
	v_mfma_f32_16x16x32_bf16 v[88:91], v[172:175], v[212:215], v[88:91]
	v_mfma_f32_16x16x32_bf16 v[76:79], v[156:159], v[220:223], v[76:79]
	v_mfma_f32_16x16x32_bf16 v[72:75], v[172:175], v[220:223], v[72:75]
	s_setprio 0
	s_setprio 1
	v_mfma_f32_16x16x32_bf16 v[116:119], v[176:179], v[192:195], v[116:119]
	v_mfma_f32_16x16x32_bf16 v[112:115], v[184:187], v[192:195], v[112:115]
	v_mfma_f32_16x16x32_bf16 v[100:103], v[176:179], v[200:203], v[100:103]
	v_mfma_f32_16x16x32_bf16 v[96:99], v[184:187], v[200:203], v[96:99]
	v_mfma_f32_16x16x32_bf16 v[84:87], v[176:179], v[208:211], v[84:87]
	v_mfma_f32_16x16x32_bf16 v[80:83], v[184:187], v[208:211], v[80:83]
	v_mfma_f32_16x16x32_bf16 v[68:71], v[176:179], v[216:219], v[68:71]
	v_mfma_f32_16x16x32_bf16 v[64:67], v[184:187], v[216:219], v[64:67]
	v_mfma_f32_16x16x32_bf16 v[116:119], v[180:183], v[196:199], v[116:119]
	v_mfma_f32_16x16x32_bf16 v[112:115], v[188:191], v[196:199], v[112:115]
	v_mfma_f32_16x16x32_bf16 v[100:103], v[180:183], v[204:207], v[100:103]
	v_mfma_f32_16x16x32_bf16 v[96:99], v[188:191], v[204:207], v[96:99]
	v_mfma_f32_16x16x32_bf16 v[84:87], v[180:183], v[212:215], v[84:87]
	v_mfma_f32_16x16x32_bf16 v[80:83], v[188:191], v[212:215], v[80:83]
	v_mfma_f32_16x16x32_bf16 v[68:71], v[180:183], v[220:223], v[68:71]
	v_mfma_f32_16x16x32_bf16 v[64:67], v[188:191], v[220:223], v[64:67]
	s_setprio 0
	s_barrier
	s_cmp_gt_u32 s0, 12
	s_cselect_b64 s[6:7], -1, 0
	s_and_b64 s[34:35], s[6:7], exec
	s_cselect_b32 s34, -13, 3
	s_cselect_b32 vcc_hi, s75, s83
	s_cselect_b32 vcc_lo, s74, s82
	s_add_i32 s34, s34, s0
	s_ashr_i32 s35, s34, 31
	s_lshl_b64 s[34:35], s[34:35], 7
	s_add_u32 vcc_lo, vcc_lo, s34
	s_addc_u32 vcc_hi, vcc_hi, s35
	s_add_i32 s39, s39, s29
	v_lshl_add_u64 v[160:161], vcc, 0, v[134:135]
	s_mov_b32 m0, s39
	ds_read_b128 v[192:195], v166 offset:49152
	ds_read_b128 v[196:199], v166 offset:50176
	ds_read_b128 v[200:203], v166 offset:51200
	ds_read_b128 v[204:207], v166 offset:52224
	ds_read_b128 v[208:211], v166 offset:53248
	ds_read_b128 v[212:215], v166 offset:54272
	ds_read_b128 v[216:219], v166 offset:55296
	ds_read_b128 v[220:223], v166 offset:56320
	global_load_lds_dwordx4 v[160:161], off
	s_add_i32 m0, s39, 0x2000
	v_lshl_add_u64 v[160:161], vcc, 0, v[138:139]
	s_add_u32 vcc_lo, vcc_lo, 0x40000
	s_addc_u32 vcc_hi, vcc_hi, 0
	s_add_i32 s39, s57, s29
	global_load_lds_dwordx4 v[160:161], off
	v_lshl_add_u64 v[160:161], vcc, 0, v[134:135]
	s_mov_b32 m0, s39
	s_nop 0
	global_load_lds_dwordx4 v[160:161], off
	s_add_i32 m0, s39, 0x2000
	s_and_b64 s[6:7], s[6:7], exec
	s_cselect_b32 s6, s60, s80
	s_cselect_b32 s7, s61, s81
	s_add_u32 s6, s6, s34
	v_lshl_add_u64 v[160:161], vcc, 0, v[138:139]
	s_addc_u32 s7, s7, s35
	global_load_lds_dwordx4 v[160:161], off
	s_mov_b32 m0, s93
	s_nop 0
	global_load_lds_dwordx4 v132, s[6:7]
	s_mov_b32 m0, s94
	s_nop 0
	global_load_lds_dwordx4 v136, s[6:7]
	s_waitcnt vmcnt(8)
	s_waitcnt lgkmcnt(0)
	s_barrier
	s_setprio 1
	s_waitcnt lgkmcnt(0)
	v_mfma_f32_16x16x32_bf16 v[60:63], v[152:155], v[192:195], v[60:63]
	v_mfma_f32_16x16x32_bf16 v[56:59], v[168:171], v[192:195], v[56:59]
	v_mfma_f32_16x16x32_bf16 v[44:47], v[152:155], v[200:203], v[44:47]
	v_mfma_f32_16x16x32_bf16 v[40:43], v[168:171], v[200:203], v[40:43]
	v_mfma_f32_16x16x32_bf16 v[28:31], v[152:155], v[208:211], v[28:31]
	v_mfma_f32_16x16x32_bf16 v[16:19], v[168:171], v[208:211], v[16:19]
	v_mfma_f32_16x16x32_bf16 v[8:11], v[152:155], v[216:219], v[8:11]
	v_mfma_f32_16x16x32_bf16 v[0:3], v[168:171], v[216:219], v[0:3]
	v_mfma_f32_16x16x32_bf16 v[60:63], v[156:159], v[196:199], v[60:63]
	v_mfma_f32_16x16x32_bf16 v[56:59], v[172:175], v[196:199], v[56:59]
	v_mfma_f32_16x16x32_bf16 v[44:47], v[156:159], v[204:207], v[44:47]
	v_mfma_f32_16x16x32_bf16 v[40:43], v[172:175], v[204:207], v[40:43]
	v_mfma_f32_16x16x32_bf16 v[28:31], v[156:159], v[212:215], v[28:31]
	v_mfma_f32_16x16x32_bf16 v[16:19], v[172:175], v[212:215], v[16:19]
	v_mfma_f32_16x16x32_bf16 v[8:11], v[156:159], v[220:223], v[8:11]
	v_mfma_f32_16x16x32_bf16 v[0:3], v[172:175], v[220:223], v[0:3]
	s_setprio 0
	s_setprio 1
	v_mfma_f32_16x16x32_bf16 v[52:55], v[176:179], v[192:195], v[52:55]
	v_mfma_f32_16x16x32_bf16 v[48:51], v[184:187], v[192:195], v[48:51]
	v_mfma_f32_16x16x32_bf16 v[36:39], v[176:179], v[200:203], v[36:39]
	v_mfma_f32_16x16x32_bf16 v[32:35], v[184:187], v[200:203], v[32:35]
	v_mfma_f32_16x16x32_bf16 v[24:27], v[176:179], v[208:211], v[24:27]
	v_mfma_f32_16x16x32_bf16 v[20:23], v[184:187], v[208:211], v[20:23]
	v_mfma_f32_16x16x32_bf16 v[12:15], v[176:179], v[216:219], v[12:15]
	v_mfma_f32_16x16x32_bf16 v[4:7], v[184:187], v[216:219], v[4:7]
	v_mfma_f32_16x16x32_bf16 v[52:55], v[180:183], v[196:199], v[52:55]
	v_mfma_f32_16x16x32_bf16 v[48:51], v[188:191], v[196:199], v[48:51]
	v_mfma_f32_16x16x32_bf16 v[36:39], v[180:183], v[204:207], v[36:39]
	v_mfma_f32_16x16x32_bf16 v[32:35], v[188:191], v[204:207], v[32:35]
	v_mfma_f32_16x16x32_bf16 v[24:27], v[180:183], v[212:215], v[24:27]
	v_mfma_f32_16x16x32_bf16 v[20:23], v[188:191], v[212:215], v[20:23]
	v_mfma_f32_16x16x32_bf16 v[12:15], v[180:183], v[220:223], v[12:15]
	v_mfma_f32_16x16x32_bf16 v[4:7], v[188:191], v[220:223], v[4:7]
	s_setprio 0
	s_barrier
	v_lshl_add_u64 v[128:129], v[128:129], 0, s[30:31]
	v_lshl_add_u64 v[130:131], v[130:131], 0, s[30:31]
	s_add_i32 s0, s0, 2
	s_and_b64 vcc, exec, s[36:37]
	s_cbranch_vccnz .LBB0_124
	s_andn2_b64 vcc, exec, s[10:11]
	s_cbranch_vccnz .LBB0_127
	s_barrier

.LBB0_517:
	ds_read_b128 v[76:79], v207
	ds_read_b128 v[88:91], v207 offset:1024
	ds_read_b128 v[92:95], v207 offset:2048
	ds_read_b128 v[144:147], v207 offset:3072
	ds_read_b128 v[148:151], v211
	ds_read_b128 v[152:155], v211 offset:1024
	ds_read_b128 v[156:159], v211 offset:2048
	ds_read_b128 v[160:163], v211 offset:3072
	s_add_i32 m0, s60, 0xc000
	ds_read_b128 v[198:201], v212
	ds_read_b128 v[214:217], v212 offset:1024
	ds_read_b128 v[218:221], v212 offset:2048
	ds_read_b128 v[222:225], v212 offset:3072
	ds_read_b128 v[226:229], v212 offset:4096
	ds_read_b128 v[230:233], v212 offset:5120
	ds_read_b128 v[234:237], v212 offset:6144
	ds_read_b128 v[238:241], v212 offset:7168
	global_load_lds_dwordx4 v[72:73], off
	s_add_i32 m0, s60, 0xe000
	s_nop 0
	global_load_lds_dwordx4 v[74:75], off
	s_waitcnt vmcnt(8)
	s_waitcnt lgkmcnt(0)
	s_barrier
	s_setprio 1
	s_waitcnt lgkmcnt(0)
	v_mfma_f32_16x16x32_bf16 v[140:143], v[76:79], v[198:201], v[140:143]
	v_mfma_f32_16x16x32_bf16 v[136:139], v[92:95], v[198:201], v[136:139]
	v_mfma_f32_16x16x32_bf16 v[124:127], v[76:79], v[218:221], v[124:127]
	v_mfma_f32_16x16x32_bf16 v[120:123], v[92:95], v[218:221], v[120:123]
	v_mfma_f32_16x16x32_bf16 v[108:111], v[76:79], v[226:229], v[108:111]
	v_mfma_f32_16x16x32_bf16 v[104:107], v[92:95], v[226:229], v[104:107]
	v_mfma_f32_16x16x32_bf16 v[84:87], v[76:79], v[234:237], v[84:87]
	v_mfma_f32_16x16x32_bf16 v[80:83], v[92:95], v[234:237], v[80:83]
	v_mfma_f32_16x16x32_bf16 v[140:143], v[88:91], v[214:217], v[140:143]
	v_mfma_f32_16x16x32_bf16 v[136:139], v[144:147], v[214:217], v[136:139]
	v_mfma_f32_16x16x32_bf16 v[124:127], v[88:91], v[222:225], v[124:127]
	v_mfma_f32_16x16x32_bf16 v[120:123], v[144:147], v[222:225], v[120:123]
	v_mfma_f32_16x16x32_bf16 v[108:111], v[88:91], v[230:233], v[108:111]
	v_mfma_f32_16x16x32_bf16 v[104:107], v[144:147], v[230:233], v[104:107]
	v_mfma_f32_16x16x32_bf16 v[84:87], v[88:91], v[238:241], v[84:87]
	v_mfma_f32_16x16x32_bf16 v[80:83], v[144:147], v[238:241], v[80:83]
	s_setprio 0
	s_setprio 1
	v_mfma_f32_16x16x32_bf16 v[132:135], v[148:151], v[198:201], v[132:135]
	v_mfma_f32_16x16x32_bf16 v[128:131], v[156:159], v[198:201], v[128:131]
	v_mfma_f32_16x16x32_bf16 v[116:119], v[148:151], v[218:221], v[116:119]
	v_mfma_f32_16x16x32_bf16 v[112:115], v[156:159], v[218:221], v[112:115]
	v_mfma_f32_16x16x32_bf16 v[100:103], v[148:151], v[226:229], v[100:103]
	v_mfma_f32_16x16x32_bf16 v[96:99], v[156:159], v[226:229], v[96:99]
	v_mfma_f32_16x16x32_bf16 v[68:71], v[148:151], v[234:237], v[68:71]
	v_mfma_f32_16x16x32_bf16 v[64:67], v[156:159], v[234:237], v[64:67]
	v_mfma_f32_16x16x32_bf16 v[132:135], v[152:155], v[214:217], v[132:135]
	v_mfma_f32_16x16x32_bf16 v[128:131], v[160:163], v[214:217], v[128:131]
	v_mfma_f32_16x16x32_bf16 v[116:119], v[152:155], v[222:225], v[116:119]
	v_mfma_f32_16x16x32_bf16 v[112:115], v[160:163], v[222:225], v[112:115]
	v_mfma_f32_16x16x32_bf16 v[100:103], v[152:155], v[230:233], v[100:103]
	v_mfma_f32_16x16x32_bf16 v[96:99], v[160:163], v[230:233], v[96:99]
	v_mfma_f32_16x16x32_bf16 v[68:71], v[152:155], v[238:241], v[68:71]
	v_mfma_f32_16x16x32_bf16 v[64:67], v[160:163], v[238:241], v[64:67]
	s_setprio 0
	s_barrier
	s_cmp_gt_u32 s35, 13
	s_cselect_b64 s[76:77], -1, 0
	s_and_b64 s[36:37], s[76:77], exec
	v_sub_co_u32_e64 v182, s[36:37], s35, 14
	s_nop 0
	v_readfirstlane_b32 s80, v182
	s_cselect_b32 s39, s43, s47
	s_cselect_b32 s75, s42, s46
	s_add_i32 s81, s80, 16
	s_and_b64 s[78:79], s[76:77], exec
	s_cselect_b32 s78, s80, s81
	s_ashr_i32 s79, s78, 31
	s_lshl_b64 s[78:79], s[78:79], 7
	s_add_u32 s80, s75, s78
	s_addc_u32 s81, s39, s79
	s_add_i32 s39, s73, s59
	s_mov_b32 m0, s39
	ds_read_b128 v[198:201], v212 offset:16384
	ds_read_b128 v[214:217], v212 offset:17408
	ds_read_b128 v[218:221], v212 offset:18432
	ds_read_b128 v[222:225], v212 offset:19456
	ds_read_b128 v[226:229], v212 offset:20480
	ds_read_b128 v[230:233], v212 offset:21504
	ds_read_b128 v[234:237], v212 offset:22528
	ds_read_b128 v[238:241], v212 offset:23552
	global_load_lds_dwordx4 v166, s[80:81]
	s_add_i32 m0, s39, 0x2000
	s_add_i32 s39, s74, s59
	global_load_lds_dwordx4 v170, s[80:81]
	s_add_u32 s80, s80, 0x40000
	s_addc_u32 s81, s81, 0
	s_mov_b32 m0, s39
	s_nop 0
	global_load_lds_dwordx4 v166, s[80:81]
	s_add_i32 m0, s39, 0x2000
	s_and_b64 s[76:77], s[76:77], exec
	s_cselect_b32 s75, s40, s48
	s_cselect_b32 s39, s41, s49
	s_add_u32 s76, s75, s78
	s_addc_u32 s77, s39, s79
	global_load_lds_dwordx4 v170, s[80:81]
	s_mov_b32 m0, s60
	s_nop 0
	global_load_lds_dwordx4 v164, s[76:77]
	s_mov_b32 m0, s61
	s_nop 0
	global_load_lds_dwordx4 v168, s[76:77]
	s_waitcnt vmcnt(8)
	s_waitcnt lgkmcnt(0)
	s_barrier
	s_setprio 1
	s_waitcnt lgkmcnt(0)
	v_mfma_f32_16x16x32_bf16 v[60:63], v[76:79], v[198:201], v[60:63]
	v_mfma_f32_16x16x32_bf16 v[56:59], v[92:95], v[198:201], v[56:59]
	v_mfma_f32_16x16x32_bf16 v[44:47], v[76:79], v[218:221], v[44:47]
	v_mfma_f32_16x16x32_bf16 v[40:43], v[92:95], v[218:221], v[40:43]
	v_mfma_f32_16x16x32_bf16 v[28:31], v[76:79], v[226:229], v[28:31]
	v_mfma_f32_16x16x32_bf16 v[16:19], v[92:95], v[226:229], v[16:19]
	v_mfma_f32_16x16x32_bf16 v[4:7], v[76:79], v[234:237], v[4:7]
	v_mfma_f32_16x16x32_bf16 v[0:3], v[92:95], v[234:237], v[0:3]
	v_mfma_f32_16x16x32_bf16 v[60:63], v[88:91], v[214:217], v[60:63]
	v_mfma_f32_16x16x32_bf16 v[56:59], v[144:147], v[214:217], v[56:59]
	v_mfma_f32_16x16x32_bf16 v[44:47], v[88:91], v[222:225], v[44:47]
	v_mfma_f32_16x16x32_bf16 v[40:43], v[144:147], v[222:225], v[40:43]
	v_mfma_f32_16x16x32_bf16 v[28:31], v[88:91], v[230:233], v[28:31]
	v_mfma_f32_16x16x32_bf16 v[16:19], v[144:147], v[230:233], v[16:19]
	v_mfma_f32_16x16x32_bf16 v[4:7], v[88:91], v[238:241], v[4:7]
	v_mfma_f32_16x16x32_bf16 v[0:3], v[144:147], v[238:241], v[0:3]
	s_setprio 0
	s_setprio 1
	v_mfma_f32_16x16x32_bf16 v[52:55], v[148:151], v[198:201], v[52:55]
	v_mfma_f32_16x16x32_bf16 v[48:51], v[156:159], v[198:201], v[48:51]
	v_mfma_f32_16x16x32_bf16 v[36:39], v[148:151], v[218:221], v[36:39]
	v_mfma_f32_16x16x32_bf16 v[32:35], v[156:159], v[218:221], v[32:35]
	v_mfma_f32_16x16x32_bf16 v[20:23], v[148:151], v[226:229], v[20:23]
	v_mfma_f32_16x16x32_bf16 v[24:27], v[156:159], v[226:229], v[24:27]
	v_mfma_f32_16x16x32_bf16 v[8:11], v[148:151], v[234:237], v[8:11]
	v_mfma_f32_16x16x32_bf16 v[12:15], v[156:159], v[234:237], v[12:15]
	v_mfma_f32_16x16x32_bf16 v[52:55], v[152:155], v[214:217], v[52:55]
	v_mfma_f32_16x16x32_bf16 v[48:51], v[160:163], v[214:217], v[48:51]
	v_mfma_f32_16x16x32_bf16 v[36:39], v[152:155], v[222:225], v[36:39]
	v_mfma_f32_16x16x32_bf16 v[32:35], v[160:163], v[222:225], v[32:35]
	v_mfma_f32_16x16x32_bf16 v[20:23], v[152:155], v[230:233], v[20:23]
	v_mfma_f32_16x16x32_bf16 v[24:27], v[160:163], v[230:233], v[24:27]
	v_mfma_f32_16x16x32_bf16 v[8:11], v[152:155], v[238:241], v[8:11]
	v_mfma_f32_16x16x32_bf16 v[12:15], v[160:163], v[238:241], v[12:15]
	s_setprio 0
	s_barrier
	s_add_i32 s39, 0, 0x18000
	s_add_i32 s75, 0, 0x1c000
	v_add_u32_e32 v144, s39, v189
	v_add_u32_e32 v160, s75, v189
	ds_read_b128 v[76:79], v144
	ds_read_b128 v[88:91], v144 offset:1024
	ds_read_b128 v[92:95], v144 offset:2048
	ds_read_b128 v[144:147], v144 offset:3072
	ds_read_b128 v[148:151], v160
	ds_read_b128 v[152:155], v160 offset:1024
	ds_read_b128 v[156:159], v160 offset:2048
	ds_read_b128 v[160:163], v160 offset:3072
	s_add_u32 s76, s76, 0x40000
	s_addc_u32 s77, s77, 0
	s_mov_b32 m0, s62
	ds_read_b128 v[198:201], v212 offset:32768
	ds_read_b128 v[214:217], v212 offset:33792
	ds_read_b128 v[218:221], v212 offset:34816
	ds_read_b128 v[222:225], v212 offset:35840
	ds_read_b128 v[226:229], v212 offset:36864
	ds_read_b128 v[230:233], v212 offset:37888
	ds_read_b128 v[234:237], v212 offset:38912
	ds_read_b128 v[238:241], v212 offset:39936
	global_load_lds_dwordx4 v164, s[76:77]
	s_mov_b32 m0, s63
	s_nop 0
	global_load_lds_dwordx4 v168, s[76:77]
	s_waitcnt vmcnt(8)
	s_waitcnt lgkmcnt(0)
	s_barrier
	s_setprio 1
	s_waitcnt lgkmcnt(0)
	v_mfma_f32_16x16x32_bf16 v[140:143], v[76:79], v[198:201], v[140:143]
	v_mfma_f32_16x16x32_bf16 v[136:139], v[92:95], v[198:201], v[136:139]
	v_mfma_f32_16x16x32_bf16 v[124:127], v[76:79], v[218:221], v[124:127]
	v_mfma_f32_16x16x32_bf16 v[120:123], v[92:95], v[218:221], v[120:123]
	v_mfma_f32_16x16x32_bf16 v[108:111], v[76:79], v[226:229], v[108:111]
	v_mfma_f32_16x16x32_bf16 v[104:107], v[92:95], v[226:229], v[104:107]
	v_mfma_f32_16x16x32_bf16 v[84:87], v[76:79], v[234:237], v[84:87]
	v_mfma_f32_16x16x32_bf16 v[80:83], v[92:95], v[234:237], v[80:83]
	v_mfma_f32_16x16x32_bf16 v[140:143], v[88:91], v[214:217], v[140:143]
	v_mfma_f32_16x16x32_bf16 v[136:139], v[144:147], v[214:217], v[136:139]
	v_mfma_f32_16x16x32_bf16 v[124:127], v[88:91], v[222:225], v[124:127]
	v_mfma_f32_16x16x32_bf16 v[120:123], v[144:147], v[222:225], v[120:123]
	v_mfma_f32_16x16x32_bf16 v[108:111], v[88:91], v[230:233], v[108:111]
	v_mfma_f32_16x16x32_bf16 v[104:107], v[144:147], v[230:233], v[104:107]
	v_mfma_f32_16x16x32_bf16 v[84:87], v[88:91], v[238:241], v[84:87]
	v_mfma_f32_16x16x32_bf16 v[80:83], v[144:147], v[238:241], v[80:83]
	s_setprio 0
	s_setprio 1
	v_mfma_f32_16x16x32_bf16 v[132:135], v[148:151], v[198:201], v[132:135]
	v_mfma_f32_16x16x32_bf16 v[128:131], v[156:159], v[198:201], v[128:131]
	v_mfma_f32_16x16x32_bf16 v[116:119], v[148:151], v[218:221], v[116:119]
	v_mfma_f32_16x16x32_bf16 v[112:115], v[156:159], v[218:221], v[112:115]
	v_mfma_f32_16x16x32_bf16 v[100:103], v[148:151], v[226:229], v[100:103]
	v_mfma_f32_16x16x32_bf16 v[96:99], v[156:159], v[226:229], v[96:99]
	v_mfma_f32_16x16x32_bf16 v[68:71], v[148:151], v[234:237], v[68:71]
	v_mfma_f32_16x16x32_bf16 v[64:67], v[156:159], v[234:237], v[64:67]
	v_mfma_f32_16x16x32_bf16 v[132:135], v[152:155], v[214:217], v[132:135]
	v_mfma_f32_16x16x32_bf16 v[128:131], v[160:163], v[214:217], v[128:131]
	v_mfma_f32_16x16x32_bf16 v[116:119], v[152:155], v[222:225], v[116:119]
	v_mfma_f32_16x16x32_bf16 v[112:115], v[160:163], v[222:225], v[112:115]
	v_mfma_f32_16x16x32_bf16 v[100:103], v[152:155], v[230:233], v[100:103]
	v_mfma_f32_16x16x32_bf16 v[96:99], v[160:163], v[230:233], v[96:99]
	v_mfma_f32_16x16x32_bf16 v[68:71], v[152:155], v[238:241], v[68:71]
	v_mfma_f32_16x16x32_bf16 v[64:67], v[160:163], v[238:241], v[64:67]
	s_setprio 0
	s_barrier
	s_cmp_gt_u32 s35, 12
	s_cselect_b64 s[76:77], -1, 0
	s_and_b64 s[78:79], s[76:77], exec
	s_cselect_b32 s78, -13, 3
	s_cselect_b32 s81, s43, s47
	s_cselect_b32 s80, s42, s46
	s_add_i32 s78, s78, s35
	s_ashr_i32 s79, s78, 31
	s_lshl_b64 s[78:79], s[78:79], 7
	s_add_u32 s80, s80, s78
	s_addc_u32 s81, s81, s79
	s_add_i32 s39, s39, s59
	s_mov_b32 m0, s39
	ds_read_b128 v[198:201], v212 offset:49152
	ds_read_b128 v[214:217], v212 offset:50176
	ds_read_b128 v[218:221], v212 offset:51200
	ds_read_b128 v[222:225], v212 offset:52224
	ds_read_b128 v[226:229], v212 offset:53248
	ds_read_b128 v[230:233], v212 offset:54272
	ds_read_b128 v[234:237], v212 offset:55296
	ds_read_b128 v[238:241], v212 offset:56320
	global_load_lds_dwordx4 v166, s[80:81]
	s_add_i32 m0, s39, 0x2000
	s_add_i32 s39, s75, s59
	global_load_lds_dwordx4 v170, s[80:81]
	s_add_u32 s80, s80, 0x40000
	s_addc_u32 s81, s81, 0
	s_mov_b32 m0, s39
	s_nop 0
	global_load_lds_dwordx4 v166, s[80:81]
	s_add_i32 m0, s39, 0x2000
	s_and_b64 s[76:77], s[76:77], exec
	s_cselect_b32 s75, s40, s48
	s_cselect_b32 s39, s41, s49
	s_add_u32 s76, s75, s78
	s_addc_u32 s77, s39, s79
	global_load_lds_dwordx4 v170, s[80:81]
	s_mov_b32 m0, s65
	s_nop 0
	global_load_lds_dwordx4 v164, s[76:77]
	s_mov_b32 m0, s66
	s_nop 0
	global_load_lds_dwordx4 v168, s[76:77]
	s_waitcnt vmcnt(8)
	s_waitcnt lgkmcnt(0)
	s_barrier
	s_setprio 1
	s_waitcnt lgkmcnt(0)
	v_mfma_f32_16x16x32_bf16 v[60:63], v[76:79], v[198:201], v[60:63]
	v_mfma_f32_16x16x32_bf16 v[56:59], v[92:95], v[198:201], v[56:59]
	v_mfma_f32_16x16x32_bf16 v[44:47], v[76:79], v[218:221], v[44:47]
	v_mfma_f32_16x16x32_bf16 v[40:43], v[92:95], v[218:221], v[40:43]
	v_mfma_f32_16x16x32_bf16 v[28:31], v[76:79], v[226:229], v[28:31]
	v_mfma_f32_16x16x32_bf16 v[16:19], v[92:95], v[226:229], v[16:19]
	v_mfma_f32_16x16x32_bf16 v[4:7], v[76:79], v[234:237], v[4:7]
	v_mfma_f32_16x16x32_bf16 v[0:3], v[92:95], v[234:237], v[0:3]
	v_mfma_f32_16x16x32_bf16 v[60:63], v[88:91], v[214:217], v[60:63]
	v_mfma_f32_16x16x32_bf16 v[56:59], v[144:147], v[214:217], v[56:59]
	v_mfma_f32_16x16x32_bf16 v[44:47], v[88:91], v[222:225], v[44:47]
	v_mfma_f32_16x16x32_bf16 v[40:43], v[144:147], v[222:225], v[40:43]
	v_mfma_f32_16x16x32_bf16 v[28:31], v[88:91], v[230:233], v[28:31]
	v_mfma_f32_16x16x32_bf16 v[16:19], v[144:147], v[230:233], v[16:19]
	v_mfma_f32_16x16x32_bf16 v[4:7], v[88:91], v[238:241], v[4:7]
	v_mfma_f32_16x16x32_bf16 v[0:3], v[144:147], v[238:241], v[0:3]
	s_setprio 0
	s_setprio 1
	v_mfma_f32_16x16x32_bf16 v[52:55], v[148:151], v[198:201], v[52:55]
	v_mfma_f32_16x16x32_bf16 v[48:51], v[156:159], v[198:201], v[48:51]
	v_mfma_f32_16x16x32_bf16 v[36:39], v[148:151], v[218:221], v[36:39]
	v_mfma_f32_16x16x32_bf16 v[32:35], v[156:159], v[218:221], v[32:35]
	v_mfma_f32_16x16x32_bf16 v[20:23], v[148:151], v[226:229], v[20:23]
	v_mfma_f32_16x16x32_bf16 v[24:27], v[156:159], v[226:229], v[24:27]
	v_mfma_f32_16x16x32_bf16 v[8:11], v[148:151], v[234:237], v[8:11]
	v_mfma_f32_16x16x32_bf16 v[12:15], v[156:159], v[234:237], v[12:15]
	v_mfma_f32_16x16x32_bf16 v[52:55], v[152:155], v[214:217], v[52:55]
	v_mfma_f32_16x16x32_bf16 v[48:51], v[160:163], v[214:217], v[48:51]
	v_mfma_f32_16x16x32_bf16 v[36:39], v[152:155], v[222:225], v[36:39]
	v_mfma_f32_16x16x32_bf16 v[32:35], v[160:163], v[222:225], v[32:35]
	v_mfma_f32_16x16x32_bf16 v[20:23], v[152:155], v[230:233], v[20:23]
	v_mfma_f32_16x16x32_bf16 v[24:27], v[160:163], v[230:233], v[24:27]
	v_mfma_f32_16x16x32_bf16 v[8:11], v[152:155], v[238:241], v[8:11]
	v_mfma_f32_16x16x32_bf16 v[12:15], v[160:163], v[238:241], v[12:15]
	s_setprio 0
	s_barrier
	v_lshl_add_u64 v[72:73], v[72:73], 0, s[30:31]
	v_lshl_add_u64 v[74:75], v[74:75], 0, s[30:31]
	s_add_i32 s35, s35, 2
	s_and_b64 vcc, exec, s[36:37]
	s_cbranch_vccnz .LBB0_517
	s_andn2_b64 vcc, exec, s[26:27]
	s_cbranch_vccnz .LBB0_520
	s_barrier

.LBB0_673:
	ds_read_b128 v[24:27], v187
	ds_read_b128 v[28:31], v187 offset:1024
	ds_read_b128 v[16:19], v187 offset:2048
	ds_read_b128 v[20:23], v187 offset:3072
	s_waitcnt lgkmcnt(0)
	ds_read_b128 v[8:11], v188
	ds_read_b128 v[12:15], v188 offset:1024
	ds_read_b128 v[0:3], v188 offset:2048
	ds_read_b128 v[4:7], v188 offset:3072
	s_add_i32 m0, s49, 0xc000
	ds_read_b128 v[192:195], v189
	ds_read_b128 v[196:199], v189 offset:1024
	ds_read_b128 v[200:203], v189 offset:2048
	ds_read_b128 v[204:207], v189 offset:3072
	ds_read_b128 v[208:211], v189 offset:4096
	ds_read_b128 v[212:215], v189 offset:5120
	ds_read_b128 v[224:227], v189 offset:6144
	ds_read_b128 v[228:231], v189 offset:7168
	global_load_lds_dwordx4 v[178:179], off
	s_add_i32 m0, s49, 0xe000
	s_nop 0
	global_load_lds_dwordx4 v[180:181], off
	s_waitcnt vmcnt(8)
	s_waitcnt lgkmcnt(0)
	s_barrier
	s_setprio 1
	s_waitcnt lgkmcnt(0)
	v_mfma_f32_16x16x128_f8f6f4 v[156:159], v[24:31], v[192:199], v[156:159]
	v_mfma_f32_16x16x128_f8f6f4 v[152:155], v[16:23], v[192:199], v[152:155]
	v_mfma_f32_16x16x128_f8f6f4 v[140:143], v[24:31], v[200:207], v[140:143]
	v_mfma_f32_16x16x128_f8f6f4 v[136:139], v[16:23], v[200:207], v[136:139]
	v_mfma_f32_16x16x128_f8f6f4 v[124:127], v[24:31], v[208:215], v[124:127]
	v_mfma_f32_16x16x128_f8f6f4 v[120:123], v[16:23], v[208:215], v[120:123]
	v_mfma_f32_16x16x128_f8f6f4 v[108:111], v[24:31], v[224:231], v[108:111]
	v_mfma_f32_16x16x128_f8f6f4 v[104:107], v[16:23], v[224:231], v[104:107]
	s_setprio 0
	s_setprio 1
	v_mfma_f32_16x16x128_f8f6f4 v[148:151], v[8:15], v[192:199], v[148:151]
	v_mfma_f32_16x16x128_f8f6f4 v[144:147], v[0:7], v[192:199], v[144:147]
	v_mfma_f32_16x16x128_f8f6f4 v[132:135], v[8:15], v[200:207], v[132:135]
	v_mfma_f32_16x16x128_f8f6f4 v[128:131], v[0:7], v[200:207], v[128:131]
	v_mfma_f32_16x16x128_f8f6f4 v[116:119], v[8:15], v[208:215], v[116:119]
	v_mfma_f32_16x16x128_f8f6f4 v[112:115], v[0:7], v[208:215], v[112:115]
	v_mfma_f32_16x16x128_f8f6f4 v[100:103], v[8:15], v[224:231], v[100:103]
	v_mfma_f32_16x16x128_f8f6f4 v[96:99], v[0:7], v[224:231], v[96:99]
	s_setprio 0
	s_barrier
	s_add_i32 s73, s67, 2
	s_cmp_lt_u32 s67, 20
	s_cselect_b64 s[36:37], -1, 0
	s_and_b64 s[74:75], s[36:37], exec
	s_cselect_b32 s0, 0, 0xffffffea
	s_cselect_b32 s77, s29, s39
	s_cselect_b32 s76, s28, s38
	s_add_i32 s0, s73, s0
	s_lshl_b64 s[74:75], s[0:1], 7
	s_add_u32 s76, s76, s74
	s_addc_u32 s77, s77, s75
	s_add_i32 s0, s60, s48
	s_mov_b32 m0, s0
	ds_read_b128 v[192:195], v189 offset:16384
	ds_read_b128 v[196:199], v189 offset:17408
	ds_read_b128 v[200:203], v189 offset:18432
	ds_read_b128 v[204:207], v189 offset:19456
	ds_read_b128 v[208:211], v189 offset:20480
	ds_read_b128 v[212:215], v189 offset:21504
	ds_read_b128 v[224:227], v189 offset:22528
	ds_read_b128 v[228:231], v189 offset:23552
	global_load_lds_dwordx4 v162, s[76:77]
	s_add_i32 m0, s0, 0x2000
	s_add_i32 s0, s61, s48
	global_load_lds_dwordx4 v166, s[76:77]
	s_add_u32 s76, s76, 0x58000
	s_addc_u32 s77, s77, 0
	s_mov_b32 m0, s0
	s_nop 0
	global_load_lds_dwordx4 v162, s[76:77]
	s_add_i32 m0, s0, 0x2000
	s_and_b64 vcc, s[36:37], exec
	s_cselect_b32 s36, s40, s34
	s_cselect_b32 s0, s41, s35
	s_add_u32 s36, s36, s74
	s_addc_u32 s37, s0, s75
	global_load_lds_dwordx4 v166, s[76:77]
	s_mov_b32 m0, s49
	s_nop 0
	global_load_lds_dwordx4 v160, s[36:37]
	s_mov_b32 m0, s50
	s_nop 0
	global_load_lds_dwordx4 v164, s[36:37]
	s_waitcnt vmcnt(8)
	s_waitcnt lgkmcnt(0)
	s_barrier
	s_setprio 1
	s_waitcnt lgkmcnt(0)
	v_mfma_f32_16x16x128_f8f6f4 v[92:95], v[24:31], v[192:199], v[92:95]
	v_mfma_f32_16x16x128_f8f6f4 v[88:91], v[16:23], v[192:199], v[88:91]
	v_mfma_f32_16x16x128_f8f6f4 v[76:79], v[24:31], v[200:207], v[76:79]
	v_mfma_f32_16x16x128_f8f6f4 v[72:75], v[16:23], v[200:207], v[72:75]
	v_mfma_f32_16x16x128_f8f6f4 v[56:59], v[24:31], v[208:215], v[56:59]
	v_mfma_f32_16x16x128_f8f6f4 v[48:51], v[16:23], v[208:215], v[48:51]
	v_mfma_f32_16x16x128_f8f6f4 v[36:39], v[24:31], v[224:231], v[36:39]
	v_mfma_f32_16x16x128_f8f6f4 v[32:35], v[16:23], v[224:231], v[32:35]
	s_setprio 0
	s_setprio 1
	v_mfma_f32_16x16x128_f8f6f4 v[84:87], v[8:15], v[192:199], v[84:87]
	v_mfma_f32_16x16x128_f8f6f4 v[80:83], v[0:7], v[192:199], v[80:83]
	v_mfma_f32_16x16x128_f8f6f4 v[68:71], v[8:15], v[200:207], v[68:71]
	v_mfma_f32_16x16x128_f8f6f4 v[64:67], v[0:7], v[200:207], v[64:67]
	v_mfma_f32_16x16x128_f8f6f4 v[60:63], v[8:15], v[208:215], v[60:63]
	v_mfma_f32_16x16x128_f8f6f4 v[52:55], v[0:7], v[208:215], v[52:55]
	v_mfma_f32_16x16x128_f8f6f4 v[44:47], v[8:15], v[224:231], v[44:47]
	v_mfma_f32_16x16x128_f8f6f4 v[40:43], v[0:7], v[224:231], v[40:43]
	s_setprio 0
	s_barrier
	s_add_i32 s78, 0, 0x18000
	s_add_i32 s79, 0, 0x1c000
	v_add_u32_e32 v0, s78, v183
	v_add_u32_e32 v4, s79, v183
	ds_read_b128 v[24:27], v0
	ds_read_b128 v[28:31], v0 offset:1024
	ds_read_b128 v[16:19], v0 offset:2048
	ds_read_b128 v[20:23], v0 offset:3072
	ds_read_b128 v[8:11], v4
	ds_read_b128 v[12:15], v4 offset:1024
	ds_read_b128 v[0:3], v4 offset:2048
	ds_read_b128 v[4:7], v4 offset:3072
	s_add_u32 s36, s36, 0x58000
	s_addc_u32 s37, s37, 0
	s_mov_b32 m0, s51
	ds_read_b128 v[192:195], v189 offset:32768
	ds_read_b128 v[196:199], v189 offset:33792
	ds_read_b128 v[200:203], v189 offset:34816
	ds_read_b128 v[204:207], v189 offset:35840
	ds_read_b128 v[208:211], v189 offset:36864
	ds_read_b128 v[212:215], v189 offset:37888
	ds_read_b128 v[224:227], v189 offset:38912
	ds_read_b128 v[228:231], v189 offset:39936
	global_load_lds_dwordx4 v160, s[36:37]
	s_mov_b32 m0, s56
	s_nop 0
	global_load_lds_dwordx4 v164, s[36:37]
	s_waitcnt vmcnt(8)
	s_waitcnt lgkmcnt(0)
	s_barrier
	s_setprio 1
	s_waitcnt lgkmcnt(0)
	v_mfma_f32_16x16x128_f8f6f4 v[156:159], v[24:31], v[192:199], v[156:159]
	v_mfma_f32_16x16x128_f8f6f4 v[152:155], v[16:23], v[192:199], v[152:155]
	v_mfma_f32_16x16x128_f8f6f4 v[140:143], v[24:31], v[200:207], v[140:143]
	v_mfma_f32_16x16x128_f8f6f4 v[136:139], v[16:23], v[200:207], v[136:139]
	v_mfma_f32_16x16x128_f8f6f4 v[124:127], v[24:31], v[208:215], v[124:127]
	v_mfma_f32_16x16x128_f8f6f4 v[120:123], v[16:23], v[208:215], v[120:123]
	v_mfma_f32_16x16x128_f8f6f4 v[108:111], v[24:31], v[224:231], v[108:111]
	v_mfma_f32_16x16x128_f8f6f4 v[104:107], v[16:23], v[224:231], v[104:107]
	s_setprio 0
	s_setprio 1
	v_mfma_f32_16x16x128_f8f6f4 v[148:151], v[8:15], v[192:199], v[148:151]
	v_mfma_f32_16x16x128_f8f6f4 v[144:147], v[0:7], v[192:199], v[144:147]
	v_mfma_f32_16x16x128_f8f6f4 v[132:135], v[8:15], v[200:207], v[132:135]
	v_mfma_f32_16x16x128_f8f6f4 v[128:131], v[0:7], v[200:207], v[128:131]
	v_mfma_f32_16x16x128_f8f6f4 v[116:119], v[8:15], v[208:215], v[116:119]
	v_mfma_f32_16x16x128_f8f6f4 v[112:115], v[0:7], v[208:215], v[112:115]
	v_mfma_f32_16x16x128_f8f6f4 v[100:103], v[8:15], v[224:231], v[100:103]
	v_mfma_f32_16x16x128_f8f6f4 v[96:99], v[0:7], v[224:231], v[96:99]
	s_setprio 0
	s_barrier
	s_cmp_lt_u32 s67, 19
	s_cselect_b64 s[36:37], -1, 0
	s_and_b64 s[74:75], s[36:37], exec
	s_cselect_b32 s0, 0, 0xffffffea
	s_cselect_b32 s77, s29, s39
	s_cselect_b32 s76, s28, s38
	s_add_i32 s0, s0, s67
	s_add_i32 s0, s0, 3
	s_lshl_b64 s[74:75], s[0:1], 7
	s_add_u32 s76, s76, s74
	s_addc_u32 s77, s77, s75
	s_add_i32 s0, s78, s48
	s_mov_b32 m0, s0
	ds_read_b128 v[192:195], v189 offset:49152
	ds_read_b128 v[196:199], v189 offset:50176
	ds_read_b128 v[200:203], v189 offset:51200
	ds_read_b128 v[204:207], v189 offset:52224
	ds_read_b128 v[208:211], v189 offset:53248
	ds_read_b128 v[212:215], v189 offset:54272
	ds_read_b128 v[224:227], v189 offset:55296
	ds_read_b128 v[228:231], v189 offset:56320
	global_load_lds_dwordx4 v162, s[76:77]
	s_add_i32 m0, s0, 0x2000
	s_add_i32 s0, s79, s48
	global_load_lds_dwordx4 v166, s[76:77]
	s_add_u32 s76, s76, 0x58000
	s_addc_u32 s77, s77, 0
	s_mov_b32 m0, s0
	s_nop 0
	global_load_lds_dwordx4 v162, s[76:77]
	s_add_i32 m0, s0, 0x2000
	s_and_b64 s[36:37], s[36:37], exec
	s_cselect_b32 s36, s40, s34
	s_cselect_b32 s0, s41, s35
	s_add_u32 s36, s36, s74
	s_addc_u32 s37, s0, s75
	global_load_lds_dwordx4 v166, s[76:77]
	s_mov_b32 m0, s57
	s_nop 0
	global_load_lds_dwordx4 v160, s[36:37]
	s_mov_b32 m0, s58
	s_nop 0
	global_load_lds_dwordx4 v164, s[36:37]
	s_waitcnt vmcnt(8)
	s_waitcnt lgkmcnt(0)
	s_barrier
	s_setprio 1
	s_waitcnt lgkmcnt(0)
	v_mfma_f32_16x16x128_f8f6f4 v[92:95], v[24:31], v[192:199], v[92:95]
	v_mfma_f32_16x16x128_f8f6f4 v[88:91], v[16:23], v[192:199], v[88:91]
	v_mfma_f32_16x16x128_f8f6f4 v[76:79], v[24:31], v[200:207], v[76:79]
	v_mfma_f32_16x16x128_f8f6f4 v[72:75], v[16:23], v[200:207], v[72:75]
	v_mfma_f32_16x16x128_f8f6f4 v[56:59], v[24:31], v[208:215], v[56:59]
	v_mfma_f32_16x16x128_f8f6f4 v[48:51], v[16:23], v[208:215], v[48:51]
	v_mfma_f32_16x16x128_f8f6f4 v[36:39], v[24:31], v[224:231], v[36:39]
	v_mfma_f32_16x16x128_f8f6f4 v[32:35], v[16:23], v[224:231], v[32:35]
	s_setprio 0
	s_setprio 1
	v_mfma_f32_16x16x128_f8f6f4 v[84:87], v[8:15], v[192:199], v[84:87]
	v_mfma_f32_16x16x128_f8f6f4 v[80:83], v[0:7], v[192:199], v[80:83]
	v_mfma_f32_16x16x128_f8f6f4 v[68:71], v[8:15], v[200:207], v[68:71]
	v_mfma_f32_16x16x128_f8f6f4 v[64:67], v[0:7], v[200:207], v[64:67]
	v_mfma_f32_16x16x128_f8f6f4 v[60:63], v[8:15], v[208:215], v[60:63]
	v_mfma_f32_16x16x128_f8f6f4 v[52:55], v[0:7], v[208:215], v[52:55]
	v_mfma_f32_16x16x128_f8f6f4 v[44:47], v[8:15], v[224:231], v[44:47]
	v_mfma_f32_16x16x128_f8f6f4 v[40:43], v[0:7], v[224:231], v[40:43]
	s_setprio 0
	s_barrier
	v_lshl_add_u64 v[178:179], v[178:179], 0, s[26:27]
	v_lshl_add_u64 v[180:181], v[180:181], 0, s[26:27]
	s_mov_b32 s67, s73
	s_cbranch_vccnz .LBB0_673
	s_andn2_b64 vcc, exec, s[22:23]
	s_cbranch_vccnz .LBB0_676
	s_barrier

.LBB0_746:
	ds_read_b128 v[24:27], v191
	ds_read_b128 v[28:31], v191 offset:1024
	ds_read_b128 v[16:19], v191 offset:2048
	ds_read_b128 v[20:23], v191 offset:3072
	ds_read_b128 v[8:11], v192
	ds_read_b128 v[12:15], v192 offset:1024
	ds_read_b128 v[0:3], v192 offset:2048
	ds_read_b128 v[4:7], v192 offset:3072
	s_add_i32 m0, s29, 0xc000
	ds_read_b128 v[196:199], v193
	ds_read_b128 v[200:203], v193 offset:1024
	ds_read_b128 v[204:207], v193 offset:2048
	ds_read_b128 v[208:211], v193 offset:3072
	ds_read_b128 v[212:215], v193 offset:4096
	ds_read_b128 v[216:219], v193 offset:5120
	ds_read_b128 v[224:227], v193 offset:6144
	ds_read_b128 v[228:231], v193 offset:7168
	global_load_lds_dwordx4 v[180:181], off
	s_add_i32 m0, s29, 0xe000
	s_nop 0
	global_load_lds_dwordx4 v[182:183], off
	s_waitcnt vmcnt(8)
	s_waitcnt lgkmcnt(0)
	s_barrier
	s_setprio 1
	s_waitcnt lgkmcnt(0)
	v_mfma_f32_16x16x128_f8f6f4 v[156:159], v[24:31], v[196:203], v[156:159]
	v_mfma_f32_16x16x128_f8f6f4 v[152:155], v[16:23], v[196:203], v[152:155]
	v_mfma_f32_16x16x128_f8f6f4 v[140:143], v[24:31], v[204:211], v[140:143]
	v_mfma_f32_16x16x128_f8f6f4 v[136:139], v[16:23], v[204:211], v[136:139]
	v_mfma_f32_16x16x128_f8f6f4 v[124:127], v[24:31], v[212:219], v[124:127]
	v_mfma_f32_16x16x128_f8f6f4 v[120:123], v[16:23], v[212:219], v[120:123]
	v_mfma_f32_16x16x128_f8f6f4 v[108:111], v[24:31], v[224:231], v[108:111]
	v_mfma_f32_16x16x128_f8f6f4 v[104:107], v[16:23], v[224:231], v[104:107]
	s_setprio 0
	s_setprio 1
	v_mfma_f32_16x16x128_f8f6f4 v[148:151], v[8:15], v[196:203], v[148:151]
	v_mfma_f32_16x16x128_f8f6f4 v[144:147], v[0:7], v[196:203], v[144:147]
	v_mfma_f32_16x16x128_f8f6f4 v[132:135], v[8:15], v[204:211], v[132:135]
	v_mfma_f32_16x16x128_f8f6f4 v[128:131], v[0:7], v[204:211], v[128:131]
	v_mfma_f32_16x16x128_f8f6f4 v[116:119], v[8:15], v[212:219], v[116:119]
	v_mfma_f32_16x16x128_f8f6f4 v[112:115], v[0:7], v[212:219], v[112:115]
	v_mfma_f32_16x16x128_f8f6f4 v[100:103], v[8:15], v[224:231], v[100:103]
	v_mfma_f32_16x16x128_f8f6f4 v[96:99], v[0:7], v[224:231], v[96:99]
	s_setprio 0
	s_barrier
	s_cmp_gt_u32 s15, 5
	s_cselect_b64 s[36:37], -1, 0
	s_and_b64 s[38:39], s[36:37], exec
	v_sub_co_u32_e64 v168, s[38:39], s15, 6
	s_nop 0
	v_readfirstlane_b32 s74, v168
	s_cselect_b32 s17, s27, s31
	s_cselect_b32 s73, s26, s30
	s_add_i32 s75, s74, 8
	s_and_b64 s[66:67], s[36:37], exec
	s_cselect_b32 s66, s74, s75
	s_ashr_i32 s67, s66, 31
	s_lshl_b64 s[66:67], s[66:67], 7
	s_add_u32 s74, s73, s66
	s_addc_u32 s75, s17, s67
	s_add_i32 s17, s63, s46
	s_mov_b32 m0, s17
	ds_read_b128 v[196:199], v193 offset:16384
	ds_read_b128 v[200:203], v193 offset:17408
	ds_read_b128 v[204:207], v193 offset:18432
	ds_read_b128 v[208:211], v193 offset:19456
	ds_read_b128 v[212:215], v193 offset:20480
	ds_read_b128 v[216:219], v193 offset:21504
	ds_read_b128 v[224:227], v193 offset:22528
	ds_read_b128 v[228:231], v193 offset:23552
	global_load_lds_dwordx4 v164, s[74:75]
	s_add_i32 m0, s17, 0x2000
	s_add_i32 s17, s64, s46
	global_load_lds_dwordx4 v160, s[74:75]
	s_add_u32 s74, s74, 0x20000
	s_addc_u32 s75, s75, 0
	s_mov_b32 m0, s17
	s_nop 0
	global_load_lds_dwordx4 v164, s[74:75]
	s_add_i32 m0, s17, 0x2000
	s_and_b64 s[36:37], s[36:37], exec
	s_cselect_b32 s36, s22, s34
	s_cselect_b32 s17, s23, s35
	s_add_u32 s36, s36, s66
	s_addc_u32 s37, s17, s67
	global_load_lds_dwordx4 v160, s[74:75]
	s_mov_b32 m0, s29
	s_nop 0
	global_load_lds_dwordx4 v166, s[36:37]
	s_mov_b32 m0, s49
	s_nop 0
	global_load_lds_dwordx4 v162, s[36:37]
	s_waitcnt vmcnt(8)
	s_waitcnt lgkmcnt(0)
	s_barrier
	s_setprio 1
	s_waitcnt lgkmcnt(0)
	v_mfma_f32_16x16x128_f8f6f4 v[92:95], v[24:31], v[196:203], v[92:95]
	v_mfma_f32_16x16x128_f8f6f4 v[88:91], v[16:23], v[196:203], v[88:91]
	v_mfma_f32_16x16x128_f8f6f4 v[76:79], v[24:31], v[204:211], v[76:79]
	v_mfma_f32_16x16x128_f8f6f4 v[72:75], v[16:23], v[204:211], v[72:75]
	v_mfma_f32_16x16x128_f8f6f4 v[52:55], v[24:31], v[212:219], v[52:55]
	v_mfma_f32_16x16x128_f8f6f4 v[48:51], v[16:23], v[212:219], v[48:51]
	v_mfma_f32_16x16x128_f8f6f4 v[36:39], v[24:31], v[224:231], v[36:39]
	v_mfma_f32_16x16x128_f8f6f4 v[32:35], v[16:23], v[224:231], v[32:35]
	s_setprio 0
	s_setprio 1
	v_mfma_f32_16x16x128_f8f6f4 v[84:87], v[8:15], v[196:203], v[84:87]
	v_mfma_f32_16x16x128_f8f6f4 v[80:83], v[0:7], v[196:203], v[80:83]
	v_mfma_f32_16x16x128_f8f6f4 v[68:71], v[8:15], v[204:211], v[68:71]
	v_mfma_f32_16x16x128_f8f6f4 v[60:63], v[0:7], v[204:211], v[60:63]
	v_mfma_f32_16x16x128_f8f6f4 v[64:67], v[8:15], v[212:219], v[64:67]
	v_mfma_f32_16x16x128_f8f6f4 v[56:59], v[0:7], v[212:219], v[56:59]
	v_mfma_f32_16x16x128_f8f6f4 v[44:47], v[8:15], v[224:231], v[44:47]
	v_mfma_f32_16x16x128_f8f6f4 v[40:43], v[0:7], v[224:231], v[40:43]
	s_setprio 0
	s_barrier
	s_add_i32 s17, 0, 0x18000
	s_add_i32 s73, 0, 0x1c000
	v_add_u32_e32 v0, s17, v188
	v_add_u32_e32 v4, s73, v188
	ds_read_b128 v[24:27], v0
	ds_read_b128 v[28:31], v0 offset:1024
	ds_read_b128 v[16:19], v0 offset:2048
	ds_read_b128 v[20:23], v0 offset:3072
	ds_read_b128 v[8:11], v4
	ds_read_b128 v[12:15], v4 offset:1024
	ds_read_b128 v[0:3], v4 offset:2048
	ds_read_b128 v[4:7], v4 offset:3072
	s_add_u32 s36, s36, 0x20000
	s_addc_u32 s37, s37, 0
	s_mov_b32 m0, s50
	ds_read_b128 v[196:199], v193 offset:32768
	ds_read_b128 v[200:203], v193 offset:33792
	ds_read_b128 v[204:207], v193 offset:34816
	ds_read_b128 v[208:211], v193 offset:35840
	ds_read_b128 v[212:215], v193 offset:36864
	ds_read_b128 v[216:219], v193 offset:37888
	ds_read_b128 v[224:227], v193 offset:38912
	ds_read_b128 v[228:231], v193 offset:39936
	global_load_lds_dwordx4 v166, s[36:37]
	s_mov_b32 m0, s51
	s_nop 0
	global_load_lds_dwordx4 v162, s[36:37]
	s_waitcnt vmcnt(8)
	s_waitcnt lgkmcnt(0)
	s_barrier
	s_setprio 1
	s_waitcnt lgkmcnt(0)
	v_mfma_f32_16x16x128_f8f6f4 v[156:159], v[24:31], v[196:203], v[156:159]
	v_mfma_f32_16x16x128_f8f6f4 v[152:155], v[16:23], v[196:203], v[152:155]
	v_mfma_f32_16x16x128_f8f6f4 v[140:143], v[24:31], v[204:211], v[140:143]
	v_mfma_f32_16x16x128_f8f6f4 v[136:139], v[16:23], v[204:211], v[136:139]
	v_mfma_f32_16x16x128_f8f6f4 v[124:127], v[24:31], v[212:219], v[124:127]
	v_mfma_f32_16x16x128_f8f6f4 v[120:123], v[16:23], v[212:219], v[120:123]
	v_mfma_f32_16x16x128_f8f6f4 v[108:111], v[24:31], v[224:231], v[108:111]
	v_mfma_f32_16x16x128_f8f6f4 v[104:107], v[16:23], v[224:231], v[104:107]
	s_setprio 0
	s_setprio 1
	v_mfma_f32_16x16x128_f8f6f4 v[148:151], v[8:15], v[196:203], v[148:151]
	v_mfma_f32_16x16x128_f8f6f4 v[144:147], v[0:7], v[196:203], v[144:147]
	v_mfma_f32_16x16x128_f8f6f4 v[132:135], v[8:15], v[204:211], v[132:135]
	v_mfma_f32_16x16x128_f8f6f4 v[128:131], v[0:7], v[204:211], v[128:131]
	v_mfma_f32_16x16x128_f8f6f4 v[116:119], v[8:15], v[212:219], v[116:119]
	v_mfma_f32_16x16x128_f8f6f4 v[112:115], v[0:7], v[212:219], v[112:115]
	v_mfma_f32_16x16x128_f8f6f4 v[100:103], v[8:15], v[224:231], v[100:103]
	v_mfma_f32_16x16x128_f8f6f4 v[96:99], v[0:7], v[224:231], v[96:99]
	s_setprio 0
	s_barrier
	s_cmp_gt_u32 s15, 4
	s_cselect_b64 s[36:37], -1, 0
	s_and_b64 s[66:67], s[36:37], exec
	s_cselect_b32 s66, -5, 3
	s_cselect_b32 s75, s27, s31
	s_cselect_b32 s74, s26, s30
	s_add_i32 s66, s66, s15
	s_ashr_i32 s67, s66, 31
	s_lshl_b64 s[66:67], s[66:67], 7
	s_add_u32 s74, s74, s66
	s_addc_u32 s75, s75, s67
	s_add_i32 s17, s17, s46
	s_mov_b32 m0, s17
	ds_read_b128 v[196:199], v193 offset:49152
	ds_read_b128 v[200:203], v193 offset:50176
	ds_read_b128 v[204:207], v193 offset:51200
	ds_read_b128 v[208:211], v193 offset:52224
	ds_read_b128 v[212:215], v193 offset:53248
	ds_read_b128 v[216:219], v193 offset:54272
	ds_read_b128 v[224:227], v193 offset:55296
	ds_read_b128 v[228:231], v193 offset:56320
	global_load_lds_dwordx4 v164, s[74:75]
	s_add_i32 m0, s17, 0x2000
	s_add_i32 s17, s73, s46
	global_load_lds_dwordx4 v160, s[74:75]
	s_add_u32 s74, s74, 0x20000
	s_addc_u32 s75, s75, 0
	s_mov_b32 m0, s17
	s_nop 0
	global_load_lds_dwordx4 v164, s[74:75]
	s_add_i32 m0, s17, 0x2000
	s_and_b64 s[36:37], s[36:37], exec
	s_cselect_b32 s36, s22, s34
	s_cselect_b32 s17, s23, s35
	s_add_u32 s36, s36, s66
	s_addc_u32 s37, s17, s67
	global_load_lds_dwordx4 v160, s[74:75]
	s_mov_b32 m0, s59
	s_nop 0
	global_load_lds_dwordx4 v166, s[36:37]
	s_mov_b32 m0, s60
	s_nop 0
	global_load_lds_dwordx4 v162, s[36:37]
	s_waitcnt vmcnt(8)
	s_waitcnt lgkmcnt(0)
	s_barrier
	s_setprio 1
	s_waitcnt lgkmcnt(0)
	v_mfma_f32_16x16x128_f8f6f4 v[92:95], v[24:31], v[196:203], v[92:95]
	v_mfma_f32_16x16x128_f8f6f4 v[88:91], v[16:23], v[196:203], v[88:91]
	v_mfma_f32_16x16x128_f8f6f4 v[76:79], v[24:31], v[204:211], v[76:79]
	v_mfma_f32_16x16x128_f8f6f4 v[72:75], v[16:23], v[204:211], v[72:75]
	v_mfma_f32_16x16x128_f8f6f4 v[52:55], v[24:31], v[212:219], v[52:55]
	v_mfma_f32_16x16x128_f8f6f4 v[48:51], v[16:23], v[212:219], v[48:51]
	v_mfma_f32_16x16x128_f8f6f4 v[36:39], v[24:31], v[224:231], v[36:39]
	v_mfma_f32_16x16x128_f8f6f4 v[32:35], v[16:23], v[224:231], v[32:35]
	s_setprio 0
	s_setprio 1
	v_mfma_f32_16x16x128_f8f6f4 v[84:87], v[8:15], v[196:203], v[84:87]
	v_mfma_f32_16x16x128_f8f6f4 v[80:83], v[0:7], v[196:203], v[80:83]
	v_mfma_f32_16x16x128_f8f6f4 v[68:71], v[8:15], v[204:211], v[68:71]
	v_mfma_f32_16x16x128_f8f6f4 v[60:63], v[0:7], v[204:211], v[60:63]
	v_mfma_f32_16x16x128_f8f6f4 v[64:67], v[8:15], v[212:219], v[64:67]
	v_mfma_f32_16x16x128_f8f6f4 v[56:59], v[0:7], v[212:219], v[56:59]
	v_mfma_f32_16x16x128_f8f6f4 v[44:47], v[8:15], v[224:231], v[44:47]
	v_mfma_f32_16x16x128_f8f6f4 v[40:43], v[0:7], v[224:231], v[40:43]
	s_setprio 0
	s_barrier
	v_lshl_add_u64 v[180:181], v[180:181], 0, s[12:13]
	v_lshl_add_u64 v[182:183], v[182:183], 0, s[12:13]
	s_add_i32 s15, s15, 2
	s_and_b64 vcc, exec, s[38:39]
	s_cbranch_vccnz .LBB0_746
	s_andn2_b64 vcc, exec, s[8:9]
	s_cbranch_vccnz .LBB0_749
	s_barrier

.LBB0_773:
	ds_read_b128 v[24:27], v200
	ds_read_b128 v[28:31], v200 offset:1024
	ds_read_b128 v[16:19], v200 offset:2048
	ds_read_b128 v[20:23], v200 offset:3072
	ds_read_b128 v[8:11], v201
	ds_read_b128 v[12:15], v201 offset:1024
	ds_read_b128 v[0:3], v201 offset:2048
	ds_read_b128 v[4:7], v201 offset:3072
	s_add_i32 m0, s39, 0xc000
	ds_read_b128 v[206:209], v202
	ds_read_b128 v[210:213], v202 offset:1024
	ds_read_b128 v[214:217], v202 offset:2048
	ds_read_b128 v[218:221], v202 offset:3072
	ds_read_b128 v[224:227], v202 offset:4096
	ds_read_b128 v[228:231], v202 offset:5120
	ds_read_b128 v[232:235], v202 offset:6144
	ds_read_b128 v[236:239], v202 offset:7168
	global_load_lds_dwordx4 v[194:195], off
	s_add_i32 m0, s39, 0xe000
	s_nop 0
	global_load_lds_dwordx4 v[196:197], off
	s_waitcnt vmcnt(8)
	s_waitcnt lgkmcnt(0)
	s_barrier
	s_setprio 1
	s_waitcnt lgkmcnt(0)
	v_mfma_f32_16x16x128_f8f6f4 v[156:159], v[24:31], v[206:213], v[156:159]
	v_mfma_f32_16x16x128_f8f6f4 v[152:155], v[16:23], v[206:213], v[152:155]
	v_mfma_f32_16x16x128_f8f6f4 v[144:147], v[24:31], v[214:221], v[144:147]
	v_mfma_f32_16x16x128_f8f6f4 v[136:139], v[16:23], v[214:221], v[136:139]
	v_mfma_f32_16x16x128_f8f6f4 v[128:131], v[24:31], v[224:231], v[128:131]
	v_mfma_f32_16x16x128_f8f6f4 v[120:123], v[16:23], v[224:231], v[120:123]
	v_mfma_f32_16x16x128_f8f6f4 v[112:115], v[24:31], v[232:239], v[112:115]
	v_mfma_f32_16x16x128_f8f6f4 v[104:107], v[16:23], v[232:239], v[104:107]
	s_setprio 0
	s_setprio 1
	v_mfma_f32_16x16x128_f8f6f4 v[148:151], v[8:15], v[206:213], v[148:151]
	v_mfma_f32_16x16x128_f8f6f4 v[140:143], v[0:7], v[206:213], v[140:143]
	v_mfma_f32_16x16x128_f8f6f4 v[132:135], v[8:15], v[214:221], v[132:135]
	v_mfma_f32_16x16x128_f8f6f4 v[124:127], v[0:7], v[214:221], v[124:127]
	v_mfma_f32_16x16x128_f8f6f4 v[116:119], v[8:15], v[224:231], v[116:119]
	v_mfma_f32_16x16x128_f8f6f4 v[108:111], v[0:7], v[224:231], v[108:111]
	v_mfma_f32_16x16x128_f8f6f4 v[100:103], v[8:15], v[232:239], v[100:103]
	v_mfma_f32_16x16x128_f8f6f4 v[96:99], v[0:7], v[232:239], v[96:99]
	s_setprio 0
	s_barrier
	s_cmp_gt_u32 s9, 5
	s_cselect_b64 s[34:35], -1, 0
	s_and_b64 s[30:31], s[34:35], exec
	v_sub_co_u32_e64 v205, s[30:31], s9, 6
	s_nop 0
	v_readfirstlane_b32 s63, v205
	s_cselect_b32 s17, s23, s27
	s_cselect_b32 s62, s22, s26
	s_add_i32 s64, s63, 8
	s_and_b64 s[60:61], s[34:35], exec
	s_cselect_b32 s60, s63, s64
	s_ashr_i32 s61, s60, 31
	s_lshl_b64 s[60:61], s[60:61], 7
	s_add_u32 s62, s62, s60
	s_addc_u32 s63, s17, s61
	s_add_i32 s17, s57, s38
	s_mov_b32 m0, s17
	ds_read_b128 v[206:209], v202 offset:16384
	ds_read_b128 v[210:213], v202 offset:17408
	ds_read_b128 v[214:217], v202 offset:18432
	ds_read_b128 v[218:221], v202 offset:19456
	ds_read_b128 v[224:227], v202 offset:20480
	ds_read_b128 v[228:231], v202 offset:21504
	ds_read_b128 v[232:235], v202 offset:22528
	ds_read_b128 v[236:239], v202 offset:23552
	global_load_lds_dwordx4 v162, s[62:63]
	s_add_i32 m0, s17, 0x2000
	s_add_i32 s17, s58, s38
	global_load_lds_dwordx4 v166, s[62:63]
	s_add_u32 s62, s62, 0x20000
	s_addc_u32 s63, s63, 0
	s_mov_b32 m0, s17
	s_nop 0
	global_load_lds_dwordx4 v162, s[62:63]
	s_add_i32 m0, s17, 0x2000
	s_and_b64 s[34:35], s[34:35], exec
	s_cselect_b32 s34, s18, s28
	s_cselect_b32 s17, s19, s29
	s_add_u32 s34, s34, s60
	s_addc_u32 s35, s17, s61
	global_load_lds_dwordx4 v166, s[62:63]
	s_mov_b32 m0, s39
	s_nop 0
	global_load_lds_dwordx4 v160, s[34:35]
	s_mov_b32 m0, s42
	s_nop 0
	global_load_lds_dwordx4 v164, s[34:35]
	s_waitcnt vmcnt(8)
	s_waitcnt lgkmcnt(0)
	s_barrier
	s_setprio 1
	s_waitcnt lgkmcnt(0)
	v_mfma_f32_16x16x128_f8f6f4 v[92:95], v[24:31], v[206:213], v[92:95]
	v_mfma_f32_16x16x128_f8f6f4 v[88:91], v[16:23], v[206:213], v[88:91]
	v_mfma_f32_16x16x128_f8f6f4 v[80:83], v[24:31], v[214:221], v[80:83]
	v_mfma_f32_16x16x128_f8f6f4 v[64:67], v[16:23], v[214:221], v[64:67]
	v_mfma_f32_16x16x128_f8f6f4 v[48:51], v[24:31], v[224:231], v[48:51]
	v_mfma_f32_16x16x128_f8f6f4 v[40:43], v[16:23], v[224:231], v[40:43]
	v_mfma_f32_16x16x128_f8f6f4 v[36:39], v[24:31], v[232:239], v[36:39]
	v_mfma_f32_16x16x128_f8f6f4 v[32:35], v[16:23], v[232:239], v[32:35]
	s_setprio 0
	s_setprio 1
	v_mfma_f32_16x16x128_f8f6f4 v[84:87], v[8:15], v[206:213], v[84:87]
	v_mfma_f32_16x16x128_f8f6f4 v[76:79], v[0:7], v[206:213], v[76:79]
	v_mfma_f32_16x16x128_f8f6f4 v[52:55], v[8:15], v[214:221], v[52:55]
	v_mfma_f32_16x16x128_f8f6f4 v[44:47], v[0:7], v[214:221], v[44:47]
	v_mfma_f32_16x16x128_f8f6f4 v[72:75], v[8:15], v[224:231], v[72:75]
	v_mfma_f32_16x16x128_f8f6f4 v[68:71], v[0:7], v[224:231], v[68:71]
	v_mfma_f32_16x16x128_f8f6f4 v[60:63], v[8:15], v[232:239], v[60:63]
	v_mfma_f32_16x16x128_f8f6f4 v[56:59], v[0:7], v[232:239], v[56:59]
	s_setprio 0
	s_barrier
	s_add_i32 s17, 0, 0x18000
	s_add_i32 s64, 0, 0x1c000
	v_add_u32_e32 v0, s17, v198
	v_add_u32_e32 v4, s64, v198
	ds_read_b128 v[24:27], v0
	ds_read_b128 v[28:31], v0 offset:1024
	ds_read_b128 v[16:19], v0 offset:2048
	ds_read_b128 v[20:23], v0 offset:3072
	ds_read_b128 v[8:11], v4
	ds_read_b128 v[12:15], v4 offset:1024
	ds_read_b128 v[0:3], v4 offset:2048
	ds_read_b128 v[4:7], v4 offset:3072
	s_add_u32 s34, s34, 0x20000
	s_addc_u32 s35, s35, 0
	s_mov_b32 m0, s43
	ds_read_b128 v[206:209], v202 offset:32768
	ds_read_b128 v[210:213], v202 offset:33792
	ds_read_b128 v[214:217], v202 offset:34816
	ds_read_b128 v[218:221], v202 offset:35840
	ds_read_b128 v[224:227], v202 offset:36864
	ds_read_b128 v[228:231], v202 offset:37888
	ds_read_b128 v[232:235], v202 offset:38912
	ds_read_b128 v[236:239], v202 offset:39936
	global_load_lds_dwordx4 v160, s[34:35]
	s_mov_b32 m0, s46
	s_nop 0
	global_load_lds_dwordx4 v164, s[34:35]
	s_waitcnt vmcnt(8)
	s_waitcnt lgkmcnt(0)
	s_barrier
	s_setprio 1
	s_waitcnt lgkmcnt(0)
	v_mfma_f32_16x16x128_f8f6f4 v[156:159], v[24:31], v[206:213], v[156:159]
	v_mfma_f32_16x16x128_f8f6f4 v[152:155], v[16:23], v[206:213], v[152:155]
	v_mfma_f32_16x16x128_f8f6f4 v[144:147], v[24:31], v[214:221], v[144:147]
	v_mfma_f32_16x16x128_f8f6f4 v[136:139], v[16:23], v[214:221], v[136:139]
	v_mfma_f32_16x16x128_f8f6f4 v[128:131], v[24:31], v[224:231], v[128:131]
	v_mfma_f32_16x16x128_f8f6f4 v[120:123], v[16:23], v[224:231], v[120:123]
	v_mfma_f32_16x16x128_f8f6f4 v[112:115], v[24:31], v[232:239], v[112:115]
	v_mfma_f32_16x16x128_f8f6f4 v[104:107], v[16:23], v[232:239], v[104:107]
	s_setprio 0
	s_setprio 1
	v_mfma_f32_16x16x128_f8f6f4 v[148:151], v[8:15], v[206:213], v[148:151]
	v_mfma_f32_16x16x128_f8f6f4 v[140:143], v[0:7], v[206:213], v[140:143]
	v_mfma_f32_16x16x128_f8f6f4 v[132:135], v[8:15], v[214:221], v[132:135]
	v_mfma_f32_16x16x128_f8f6f4 v[124:127], v[0:7], v[214:221], v[124:127]
	v_mfma_f32_16x16x128_f8f6f4 v[116:119], v[8:15], v[224:231], v[116:119]
	v_mfma_f32_16x16x128_f8f6f4 v[108:111], v[0:7], v[224:231], v[108:111]
	v_mfma_f32_16x16x128_f8f6f4 v[100:103], v[8:15], v[232:239], v[100:103]
	v_mfma_f32_16x16x128_f8f6f4 v[96:99], v[0:7], v[232:239], v[96:99]
	s_setprio 0
	s_barrier
	s_cmp_gt_u32 s9, 4
	s_cselect_b64 s[34:35], -1, 0
	s_and_b64 s[60:61], s[34:35], exec
	s_cselect_b32 s60, -5, 3
	s_cselect_b32 s63, s23, s27
	s_cselect_b32 s62, s22, s26
	s_add_i32 s60, s60, s9
	s_ashr_i32 s61, s60, 31
	s_lshl_b64 s[60:61], s[60:61], 7
	s_add_u32 s62, s62, s60
	s_addc_u32 s63, s63, s61
	s_add_i32 s17, s17, s38
	s_mov_b32 m0, s17
	ds_read_b128 v[206:209], v202 offset:49152
	ds_read_b128 v[210:213], v202 offset:50176
	ds_read_b128 v[214:217], v202 offset:51200
	ds_read_b128 v[218:221], v202 offset:52224
	ds_read_b128 v[224:227], v202 offset:53248
	ds_read_b128 v[228:231], v202 offset:54272
	ds_read_b128 v[232:235], v202 offset:55296
	ds_read_b128 v[236:239], v202 offset:56320
	global_load_lds_dwordx4 v162, s[62:63]
	s_add_i32 m0, s17, 0x2000
	s_add_i32 s17, s64, s38
	global_load_lds_dwordx4 v166, s[62:63]
	s_add_u32 s62, s62, 0x20000
	s_addc_u32 s63, s63, 0
	s_mov_b32 m0, s17
	s_nop 0
	global_load_lds_dwordx4 v162, s[62:63]
	s_add_i32 m0, s17, 0x2000
	s_and_b64 s[34:35], s[34:35], exec
	s_cselect_b32 s34, s18, s28
	s_cselect_b32 s17, s19, s29
	s_add_u32 s34, s34, s60
	s_addc_u32 s35, s17, s61
	global_load_lds_dwordx4 v166, s[62:63]
	s_mov_b32 m0, s49
	s_nop 0
	global_load_lds_dwordx4 v160, s[34:35]
	s_mov_b32 m0, s50
	s_nop 0
	global_load_lds_dwordx4 v164, s[34:35]
	s_waitcnt vmcnt(8)
	s_waitcnt lgkmcnt(0)
	s_barrier
	s_setprio 1
	s_waitcnt lgkmcnt(0)
	v_mfma_f32_16x16x128_f8f6f4 v[92:95], v[24:31], v[206:213], v[92:95]
	v_mfma_f32_16x16x128_f8f6f4 v[88:91], v[16:23], v[206:213], v[88:91]
	v_mfma_f32_16x16x128_f8f6f4 v[80:83], v[24:31], v[214:221], v[80:83]
	v_mfma_f32_16x16x128_f8f6f4 v[64:67], v[16:23], v[214:221], v[64:67]
	v_mfma_f32_16x16x128_f8f6f4 v[48:51], v[24:31], v[224:231], v[48:51]
	v_mfma_f32_16x16x128_f8f6f4 v[40:43], v[16:23], v[224:231], v[40:43]
	v_mfma_f32_16x16x128_f8f6f4 v[36:39], v[24:31], v[232:239], v[36:39]
	v_mfma_f32_16x16x128_f8f6f4 v[32:35], v[16:23], v[232:239], v[32:35]
	s_setprio 0
	s_setprio 1
	v_mfma_f32_16x16x128_f8f6f4 v[84:87], v[8:15], v[206:213], v[84:87]
	v_mfma_f32_16x16x128_f8f6f4 v[76:79], v[0:7], v[206:213], v[76:79]
	v_mfma_f32_16x16x128_f8f6f4 v[52:55], v[8:15], v[214:221], v[52:55]
	v_mfma_f32_16x16x128_f8f6f4 v[44:47], v[0:7], v[214:221], v[44:47]
	v_mfma_f32_16x16x128_f8f6f4 v[72:75], v[8:15], v[224:231], v[72:75]
	v_mfma_f32_16x16x128_f8f6f4 v[68:71], v[0:7], v[224:231], v[68:71]
	v_mfma_f32_16x16x128_f8f6f4 v[60:63], v[8:15], v[232:239], v[60:63]
	v_mfma_f32_16x16x128_f8f6f4 v[56:59], v[0:7], v[232:239], v[56:59]
	s_setprio 0
	s_barrier
	v_lshl_add_u64 v[194:195], v[194:195], 0, s[12:13]
	v_lshl_add_u64 v[196:197], v[196:197], 0, s[12:13]
	s_add_i32 s9, s9, 2
	s_and_b64 vcc, exec, s[30:31]
	s_cbranch_vccnz .LBB0_773
	s_andn2_b64 vcc, exec, s[10:11]
	s_cbranch_vccnz .LBB0_776
	s_barrier

.LBB0_959:
	ds_read_b128 v[24:27], v187
	ds_read_b128 v[28:31], v187 offset:1024
	ds_read_b128 v[16:19], v187 offset:2048
	ds_read_b128 v[20:23], v187 offset:3072
	s_waitcnt lgkmcnt(0)
	ds_read_b128 v[8:11], v188
	ds_read_b128 v[12:15], v188 offset:1024
	ds_read_b128 v[0:3], v188 offset:2048
	ds_read_b128 v[4:7], v188 offset:3072
	s_add_i32 m0, s49, 0xc000
	ds_read_b128 v[192:195], v189
	ds_read_b128 v[196:199], v189 offset:1024
	ds_read_b128 v[200:203], v189 offset:2048
	ds_read_b128 v[204:207], v189 offset:3072
	ds_read_b128 v[208:211], v189 offset:4096
	ds_read_b128 v[212:215], v189 offset:5120
	ds_read_b128 v[224:227], v189 offset:6144
	ds_read_b128 v[228:231], v189 offset:7168
	global_load_lds_dwordx4 v[178:179], off
	s_add_i32 m0, s49, 0xe000
	s_nop 0
	global_load_lds_dwordx4 v[180:181], off
	s_waitcnt vmcnt(8)
	s_waitcnt lgkmcnt(0)
	s_barrier
	s_setprio 1
	s_waitcnt lgkmcnt(0)
	v_mfma_f32_16x16x128_f8f6f4 v[156:159], v[24:31], v[192:199], v[156:159]
	v_mfma_f32_16x16x128_f8f6f4 v[152:155], v[16:23], v[192:199], v[152:155]
	v_mfma_f32_16x16x128_f8f6f4 v[140:143], v[24:31], v[200:207], v[140:143]
	v_mfma_f32_16x16x128_f8f6f4 v[136:139], v[16:23], v[200:207], v[136:139]
	v_mfma_f32_16x16x128_f8f6f4 v[124:127], v[24:31], v[208:215], v[124:127]
	v_mfma_f32_16x16x128_f8f6f4 v[120:123], v[16:23], v[208:215], v[120:123]
	v_mfma_f32_16x16x128_f8f6f4 v[108:111], v[24:31], v[224:231], v[108:111]
	v_mfma_f32_16x16x128_f8f6f4 v[104:107], v[16:23], v[224:231], v[104:107]
	s_setprio 0
	s_setprio 1
	v_mfma_f32_16x16x128_f8f6f4 v[148:151], v[8:15], v[192:199], v[148:151]
	v_mfma_f32_16x16x128_f8f6f4 v[144:147], v[0:7], v[192:199], v[144:147]
	v_mfma_f32_16x16x128_f8f6f4 v[132:135], v[8:15], v[200:207], v[132:135]
	v_mfma_f32_16x16x128_f8f6f4 v[128:131], v[0:7], v[200:207], v[128:131]
	v_mfma_f32_16x16x128_f8f6f4 v[116:119], v[8:15], v[208:215], v[116:119]
	v_mfma_f32_16x16x128_f8f6f4 v[112:115], v[0:7], v[208:215], v[112:115]
	v_mfma_f32_16x16x128_f8f6f4 v[100:103], v[8:15], v[224:231], v[100:103]
	v_mfma_f32_16x16x128_f8f6f4 v[96:99], v[0:7], v[224:231], v[96:99]
	s_setprio 0
	s_barrier
	s_add_i32 s23, s21, 2
	s_cmp_lt_u32 s21, 6
	s_cselect_b64 s[36:37], -1, 0
	s_and_b64 s[64:65], s[36:37], exec
	s_cselect_b32 s0, 0, -8
	s_cselect_b32 s63, s39, s35
	s_cselect_b32 s66, s38, s34
	s_add_i32 s0, s23, s0
	s_lshl_b64 s[64:65], s[0:1], 7
	s_add_u32 s66, s66, s64
	s_addc_u32 s67, s63, s65
	s_add_i32 s0, s60, s48
	s_mov_b32 m0, s0
	ds_read_b128 v[192:195], v189 offset:16384
	ds_read_b128 v[196:199], v189 offset:17408
	ds_read_b128 v[200:203], v189 offset:18432
	ds_read_b128 v[204:207], v189 offset:19456
	ds_read_b128 v[208:211], v189 offset:20480
	ds_read_b128 v[212:215], v189 offset:21504
	ds_read_b128 v[224:227], v189 offset:22528
	ds_read_b128 v[228:231], v189 offset:23552
	global_load_lds_dwordx4 v162, s[66:67]
	s_add_i32 m0, s0, 0x2000
	s_add_i32 s0, s61, s48
	global_load_lds_dwordx4 v166, s[66:67]
	s_add_u32 s66, s66, 0x20000
	s_addc_u32 s67, s67, 0
	s_mov_b32 m0, s0
	s_nop 0
	global_load_lds_dwordx4 v162, s[66:67]
	s_add_i32 m0, s0, 0x2000
	s_and_b64 vcc, s[36:37], exec
	s_cselect_b32 s36, s40, s30
	s_cselect_b32 s0, s41, s31
	s_add_u32 s36, s36, s64
	s_addc_u32 s37, s0, s65
	global_load_lds_dwordx4 v166, s[66:67]
	s_mov_b32 m0, s49
	s_nop 0
	global_load_lds_dwordx4 v160, s[36:37]
	s_mov_b32 m0, s50
	s_nop 0
	global_load_lds_dwordx4 v164, s[36:37]
	s_waitcnt vmcnt(8)
	s_waitcnt lgkmcnt(0)
	s_barrier
	s_setprio 1
	s_waitcnt lgkmcnt(0)
	v_mfma_f32_16x16x128_f8f6f4 v[92:95], v[24:31], v[192:199], v[92:95]
	v_mfma_f32_16x16x128_f8f6f4 v[88:91], v[16:23], v[192:199], v[88:91]
	v_mfma_f32_16x16x128_f8f6f4 v[76:79], v[24:31], v[200:207], v[76:79]
	v_mfma_f32_16x16x128_f8f6f4 v[72:75], v[16:23], v[200:207], v[72:75]
	v_mfma_f32_16x16x128_f8f6f4 v[56:59], v[24:31], v[208:215], v[56:59]
	v_mfma_f32_16x16x128_f8f6f4 v[48:51], v[16:23], v[208:215], v[48:51]
	v_mfma_f32_16x16x128_f8f6f4 v[36:39], v[24:31], v[224:231], v[36:39]
	v_mfma_f32_16x16x128_f8f6f4 v[32:35], v[16:23], v[224:231], v[32:35]
	s_setprio 0
	s_setprio 1
	v_mfma_f32_16x16x128_f8f6f4 v[84:87], v[8:15], v[192:199], v[84:87]
	v_mfma_f32_16x16x128_f8f6f4 v[80:83], v[0:7], v[192:199], v[80:83]
	v_mfma_f32_16x16x128_f8f6f4 v[68:71], v[8:15], v[200:207], v[68:71]
	v_mfma_f32_16x16x128_f8f6f4 v[64:67], v[0:7], v[200:207], v[64:67]
	v_mfma_f32_16x16x128_f8f6f4 v[60:63], v[8:15], v[208:215], v[60:63]
	v_mfma_f32_16x16x128_f8f6f4 v[52:55], v[0:7], v[208:215], v[52:55]
	v_mfma_f32_16x16x128_f8f6f4 v[44:47], v[8:15], v[224:231], v[44:47]
	v_mfma_f32_16x16x128_f8f6f4 v[40:43], v[0:7], v[224:231], v[40:43]
	s_setprio 0
	s_barrier
	s_add_i32 s63, 0, 0x18000
	s_add_i32 s68, 0, 0x1c000
	v_add_u32_e32 v0, s63, v183
	v_add_u32_e32 v4, s68, v183
	ds_read_b128 v[24:27], v0
	ds_read_b128 v[28:31], v0 offset:1024
	ds_read_b128 v[16:19], v0 offset:2048
	ds_read_b128 v[20:23], v0 offset:3072
	ds_read_b128 v[8:11], v4
	ds_read_b128 v[12:15], v4 offset:1024
	ds_read_b128 v[0:3], v4 offset:2048
	ds_read_b128 v[4:7], v4 offset:3072
	s_add_u32 s36, s36, 0x20000
	s_addc_u32 s37, s37, 0
	s_mov_b32 m0, s51
	ds_read_b128 v[192:195], v189 offset:32768
	ds_read_b128 v[196:199], v189 offset:33792
	ds_read_b128 v[200:203], v189 offset:34816
	ds_read_b128 v[204:207], v189 offset:35840
	ds_read_b128 v[208:211], v189 offset:36864
	ds_read_b128 v[212:215], v189 offset:37888
	ds_read_b128 v[224:227], v189 offset:38912
	ds_read_b128 v[228:231], v189 offset:39936
	global_load_lds_dwordx4 v160, s[36:37]
	s_mov_b32 m0, s56
	s_nop 0
	global_load_lds_dwordx4 v164, s[36:37]
	s_waitcnt vmcnt(8)
	s_waitcnt lgkmcnt(0)
	s_barrier
	s_setprio 1
	s_waitcnt lgkmcnt(0)
	v_mfma_f32_16x16x128_f8f6f4 v[156:159], v[24:31], v[192:199], v[156:159]
	v_mfma_f32_16x16x128_f8f6f4 v[152:155], v[16:23], v[192:199], v[152:155]
	v_mfma_f32_16x16x128_f8f6f4 v[140:143], v[24:31], v[200:207], v[140:143]
	v_mfma_f32_16x16x128_f8f6f4 v[136:139], v[16:23], v[200:207], v[136:139]
	v_mfma_f32_16x16x128_f8f6f4 v[124:127], v[24:31], v[208:215], v[124:127]
	v_mfma_f32_16x16x128_f8f6f4 v[120:123], v[16:23], v[208:215], v[120:123]
	v_mfma_f32_16x16x128_f8f6f4 v[108:111], v[24:31], v[224:231], v[108:111]
	v_mfma_f32_16x16x128_f8f6f4 v[104:107], v[16:23], v[224:231], v[104:107]
	s_setprio 0
	s_setprio 1
	v_mfma_f32_16x16x128_f8f6f4 v[148:151], v[8:15], v[192:199], v[148:151]
	v_mfma_f32_16x16x128_f8f6f4 v[144:147], v[0:7], v[192:199], v[144:147]
	v_mfma_f32_16x16x128_f8f6f4 v[132:135], v[8:15], v[200:207], v[132:135]
	v_mfma_f32_16x16x128_f8f6f4 v[128:131], v[0:7], v[200:207], v[128:131]
	v_mfma_f32_16x16x128_f8f6f4 v[116:119], v[8:15], v[208:215], v[116:119]
	v_mfma_f32_16x16x128_f8f6f4 v[112:115], v[0:7], v[208:215], v[112:115]
	v_mfma_f32_16x16x128_f8f6f4 v[100:103], v[8:15], v[224:231], v[100:103]
	v_mfma_f32_16x16x128_f8f6f4 v[96:99], v[0:7], v[224:231], v[96:99]
	s_setprio 0
	s_barrier
	s_cmp_lt_u32 s21, 5
	s_cselect_b64 s[36:37], -1, 0
	s_and_b64 s[64:65], s[36:37], exec
	s_cselect_b32 s0, 0, -8
	s_cselect_b32 s67, s39, s35
	s_cselect_b32 s66, s38, s34
	s_add_i32 s0, s0, s21
	s_add_i32 s0, s0, 3
	s_lshl_b64 s[64:65], s[0:1], 7
	s_add_u32 s66, s66, s64
	s_addc_u32 s67, s67, s65
	s_add_i32 s0, s63, s48
	s_mov_b32 m0, s0
	ds_read_b128 v[192:195], v189 offset:49152
	ds_read_b128 v[196:199], v189 offset:50176
	ds_read_b128 v[200:203], v189 offset:51200
	ds_read_b128 v[204:207], v189 offset:52224
	ds_read_b128 v[208:211], v189 offset:53248
	ds_read_b128 v[212:215], v189 offset:54272
	ds_read_b128 v[224:227], v189 offset:55296
	ds_read_b128 v[228:231], v189 offset:56320
	global_load_lds_dwordx4 v162, s[66:67]
	s_add_i32 m0, s0, 0x2000
	s_add_i32 s0, s68, s48
	global_load_lds_dwordx4 v166, s[66:67]
	s_add_u32 s66, s66, 0x20000
	s_addc_u32 s67, s67, 0
	s_mov_b32 m0, s0
	s_nop 0
	global_load_lds_dwordx4 v162, s[66:67]
	s_add_i32 m0, s0, 0x2000
	s_and_b64 s[36:37], s[36:37], exec
	s_cselect_b32 s21, s40, s30
	s_cselect_b32 s0, s41, s31
	s_add_u32 s36, s21, s64
	s_addc_u32 s37, s0, s65
	global_load_lds_dwordx4 v166, s[66:67]
	s_mov_b32 m0, s57
	s_nop 0
	global_load_lds_dwordx4 v160, s[36:37]
	s_mov_b32 m0, s58
	s_nop 0
	global_load_lds_dwordx4 v164, s[36:37]
	s_waitcnt vmcnt(8)
	s_waitcnt lgkmcnt(0)
	s_barrier
	s_setprio 1
	s_waitcnt lgkmcnt(0)
	v_mfma_f32_16x16x128_f8f6f4 v[92:95], v[24:31], v[192:199], v[92:95]
	v_mfma_f32_16x16x128_f8f6f4 v[88:91], v[16:23], v[192:199], v[88:91]
	v_mfma_f32_16x16x128_f8f6f4 v[76:79], v[24:31], v[200:207], v[76:79]
	v_mfma_f32_16x16x128_f8f6f4 v[72:75], v[16:23], v[200:207], v[72:75]
	v_mfma_f32_16x16x128_f8f6f4 v[56:59], v[24:31], v[208:215], v[56:59]
	v_mfma_f32_16x16x128_f8f6f4 v[48:51], v[16:23], v[208:215], v[48:51]
	v_mfma_f32_16x16x128_f8f6f4 v[36:39], v[24:31], v[224:231], v[36:39]
	v_mfma_f32_16x16x128_f8f6f4 v[32:35], v[16:23], v[224:231], v[32:35]
	s_setprio 0
	s_setprio 1
	v_mfma_f32_16x16x128_f8f6f4 v[84:87], v[8:15], v[192:199], v[84:87]
	v_mfma_f32_16x16x128_f8f6f4 v[80:83], v[0:7], v[192:199], v[80:83]
	v_mfma_f32_16x16x128_f8f6f4 v[68:71], v[8:15], v[200:207], v[68:71]
	v_mfma_f32_16x16x128_f8f6f4 v[64:67], v[0:7], v[200:207], v[64:67]
	v_mfma_f32_16x16x128_f8f6f4 v[60:63], v[8:15], v[208:215], v[60:63]
	v_mfma_f32_16x16x128_f8f6f4 v[52:55], v[0:7], v[208:215], v[52:55]
	v_mfma_f32_16x16x128_f8f6f4 v[44:47], v[8:15], v[224:231], v[44:47]
	v_mfma_f32_16x16x128_f8f6f4 v[40:43], v[0:7], v[224:231], v[40:43]
	s_setprio 0
	s_barrier
	v_lshl_add_u64 v[178:179], v[178:179], 0, s[16:17]
	v_lshl_add_u64 v[180:181], v[180:181], 0, s[16:17]
	s_mov_b32 s21, s23
	s_cbranch_vccnz .LBB0_959
	s_andn2_b64 vcc, exec, s[14:15]
	s_cbranch_vccnz .LBB0_962
	s_barrier

.LBB0_1263:
	ds_read_b128 v[24:27], v231
	ds_read_b128 v[28:31], v231 offset:1024
	ds_read_b128 v[16:19], v231 offset:2048
	ds_read_b128 v[20:23], v231 offset:3072
	ds_read_b128 v[8:11], v237
	ds_read_b128 v[12:15], v237 offset:1024
	ds_read_b128 v[0:3], v237 offset:2048
	ds_read_b128 v[4:7], v237 offset:3072
	s_add_i32 m0, s68, 0xc000
	ds_read_b128 v[166:169], v243
	ds_read_b128 v[170:173], v243 offset:1024
	ds_read_b128 v[174:177], v243 offset:2048
	ds_read_b128 v[178:181], v243 offset:3072
	ds_read_b128 v[182:185], v243 offset:4096
	ds_read_b128 v[186:189], v243 offset:5120
	ds_read_b128 v[216:219], v243 offset:6144
	ds_read_b128 v[220:223], v243 offset:7168
	global_load_lds_dwordx4 v[162:163], off
	s_add_i32 m0, s68, 0xe000
	s_nop 0
	global_load_lds_dwordx4 v[164:165], off
	s_waitcnt vmcnt(8)
	s_waitcnt lgkmcnt(0)
	s_barrier
	s_setprio 1
	s_waitcnt lgkmcnt(0)
	v_mfma_f32_16x16x128_f8f6f4 v[156:159], v[24:31], v[166:173], v[156:159]
	v_mfma_f32_16x16x128_f8f6f4 v[152:155], v[16:23], v[166:173], v[152:155]
	v_mfma_f32_16x16x128_f8f6f4 v[140:143], v[24:31], v[174:181], v[140:143]
	v_mfma_f32_16x16x128_f8f6f4 v[136:139], v[16:23], v[174:181], v[136:139]
	v_mfma_f32_16x16x128_f8f6f4 v[124:127], v[24:31], v[182:189], v[124:127]
	v_mfma_f32_16x16x128_f8f6f4 v[120:123], v[16:23], v[182:189], v[120:123]
	v_mfma_f32_16x16x128_f8f6f4 v[108:111], v[24:31], v[216:223], v[108:111]
	v_mfma_f32_16x16x128_f8f6f4 v[104:107], v[16:23], v[216:223], v[104:107]
	s_setprio 0
	s_setprio 1
	v_mfma_f32_16x16x128_f8f6f4 v[148:151], v[8:15], v[166:173], v[148:151]
	v_mfma_f32_16x16x128_f8f6f4 v[144:147], v[0:7], v[166:173], v[144:147]
	v_mfma_f32_16x16x128_f8f6f4 v[132:135], v[8:15], v[174:181], v[132:135]
	v_mfma_f32_16x16x128_f8f6f4 v[128:131], v[0:7], v[174:181], v[128:131]
	v_mfma_f32_16x16x128_f8f6f4 v[116:119], v[8:15], v[182:189], v[116:119]
	v_mfma_f32_16x16x128_f8f6f4 v[112:115], v[0:7], v[182:189], v[112:115]
	v_mfma_f32_16x16x128_f8f6f4 v[100:103], v[8:15], v[216:223], v[100:103]
	v_mfma_f32_16x16x128_f8f6f4 v[96:99], v[0:7], v[216:223], v[96:99]
	s_setprio 0
	s_barrier
	s_cmp_gt_u32 s43, 25
	v_sub_co_u32_e64 v200, s[40:41], s43, 26
	s_cselect_b64 vcc, -1, 0
	v_add_u32_e32 v210, 28, v200
	v_cndmask_b32_e32 v224, v210, v200, vcc
	v_ashrrev_i32_e32 v225, 31, v224
	v_cndmask_b32_e32 v191, v161, v209, vcc
	v_cndmask_b32_e32 v190, v160, v208, vcc
	v_lshlrev_b64 v[224:225], 7, v[224:225]
	v_lshl_add_u64 v[190:191], v[190:191], 0, v[224:225]
	s_add_i32 s44, s24, s66
	v_lshl_add_u64 v[228:229], v[190:191], 0, v[194:195]
	s_mov_b32 m0, s44
	ds_read_b128 v[166:169], v243 offset:16384
	ds_read_b128 v[170:173], v243 offset:17408
	ds_read_b128 v[174:177], v243 offset:18432
	ds_read_b128 v[178:181], v243 offset:19456
	ds_read_b128 v[182:185], v243 offset:20480
	ds_read_b128 v[186:189], v243 offset:21504
	ds_read_b128 v[216:219], v243 offset:22528
	ds_read_b128 v[220:223], v243 offset:23552
	global_load_lds_dwordx4 v[228:229], off
	v_lshl_add_u64 v[228:229], v[190:191], 0, v[198:199]
	s_add_i32 m0, s44, 0x2000
	v_lshl_add_u64 v[190:191], v[190:191], 0, s[0:1]
	s_add_i32 s44, s80, s66
	global_load_lds_dwordx4 v[228:229], off
	v_lshl_add_u64 v[228:229], v[190:191], 0, v[194:195]
	s_mov_b32 m0, s44
	v_lshl_add_u64 v[190:191], v[190:191], 0, v[198:199]
	global_load_lds_dwordx4 v[228:229], off
	s_add_i32 m0, s44, 0x2000
	s_and_b64 s[44:45], vcc, exec
	s_cselect_b32 s45, s63, s39
	s_cselect_b32 s44, s62, s38
	global_load_lds_dwordx4 v[190:191], off
	v_lshl_add_u64 v[190:191], s[44:45], 0, v[224:225]
	v_lshl_add_u64 v[224:225], v[190:191], 0, v[192:193]
	s_mov_b32 m0, s68
	s_nop 0
	global_load_lds_dwordx4 v[224:225], off
	v_lshl_add_u64 v[224:225], v[190:191], 0, v[196:197]
	s_mov_b32 m0, s69
	s_nop 0
	global_load_lds_dwordx4 v[224:225], off
	s_waitcnt vmcnt(8)
	s_waitcnt lgkmcnt(0)
	s_barrier
	s_setprio 1
	s_waitcnt lgkmcnt(0)
	v_mfma_f32_16x16x128_f8f6f4 v[92:95], v[24:31], v[166:173], v[92:95]
	v_mfma_f32_16x16x128_f8f6f4 v[88:91], v[16:23], v[166:173], v[88:91]
	v_mfma_f32_16x16x128_f8f6f4 v[76:79], v[24:31], v[174:181], v[76:79]
	v_mfma_f32_16x16x128_f8f6f4 v[72:75], v[16:23], v[174:181], v[72:75]
	v_mfma_f32_16x16x128_f8f6f4 v[52:55], v[24:31], v[182:189], v[52:55]
	v_mfma_f32_16x16x128_f8f6f4 v[48:51], v[16:23], v[182:189], v[48:51]
	v_mfma_f32_16x16x128_f8f6f4 v[36:39], v[24:31], v[216:223], v[36:39]
	v_mfma_f32_16x16x128_f8f6f4 v[32:35], v[16:23], v[216:223], v[32:35]
	s_setprio 0
	s_setprio 1
	v_mfma_f32_16x16x128_f8f6f4 v[84:87], v[8:15], v[166:173], v[84:87]
	v_mfma_f32_16x16x128_f8f6f4 v[80:83], v[0:7], v[166:173], v[80:83]
	v_mfma_f32_16x16x128_f8f6f4 v[60:63], v[8:15], v[174:181], v[60:63]
	v_mfma_f32_16x16x128_f8f6f4 v[56:59], v[0:7], v[174:181], v[56:59]
	v_mfma_f32_16x16x128_f8f6f4 v[68:71], v[8:15], v[182:189], v[68:71]
	v_mfma_f32_16x16x128_f8f6f4 v[64:67], v[0:7], v[182:189], v[64:67]
	v_mfma_f32_16x16x128_f8f6f4 v[44:47], v[8:15], v[216:223], v[44:47]
	v_mfma_f32_16x16x128_f8f6f4 v[40:43], v[0:7], v[216:223], v[40:43]
	s_setprio 0
	s_barrier
	s_add_i32 s46, 0, 0x18000
	s_add_i32 s47, 0, 0x1c000
	v_add_u32_e32 v0, s46, v215
	v_add_u32_e32 v4, s47, v215
	ds_read_b128 v[16:19], v0
	ds_read_b128 v[20:23], v0 offset:1024
	ds_read_b128 v[24:27], v0 offset:2048
	ds_read_b128 v[28:31], v0 offset:3072
	ds_read_b128 v[8:11], v4
	ds_read_b128 v[12:15], v4 offset:1024
	ds_read_b128 v[0:3], v4 offset:2048
	ds_read_b128 v[4:7], v4 offset:3072
	v_lshl_add_u64 v[190:191], v[190:191], 0, s[0:1]
	s_mov_b32 m0, s70
	v_lshl_add_u64 v[224:225], v[190:191], 0, v[192:193]
	ds_read_b128 v[166:169], v243 offset:32768
	ds_read_b128 v[170:173], v243 offset:33792
	ds_read_b128 v[174:177], v243 offset:34816
	ds_read_b128 v[178:181], v243 offset:35840
	ds_read_b128 v[182:185], v243 offset:36864
	ds_read_b128 v[186:189], v243 offset:37888
	ds_read_b128 v[216:219], v243 offset:38912
	ds_read_b128 v[220:223], v243 offset:39936
	global_load_lds_dwordx4 v[224:225], off
	v_lshl_add_u64 v[190:191], v[190:191], 0, v[196:197]
	s_mov_b32 m0, s71
	s_nop 0
	global_load_lds_dwordx4 v[190:191], off
	s_waitcnt vmcnt(8)
	s_waitcnt lgkmcnt(0)
	s_barrier
	s_setprio 1
	s_waitcnt lgkmcnt(0)
	v_mfma_f32_16x16x128_f8f6f4 v[156:159], v[16:23], v[166:173], v[156:159]
	v_mfma_f32_16x16x128_f8f6f4 v[152:155], v[24:31], v[166:173], v[152:155]
	v_mfma_f32_16x16x128_f8f6f4 v[140:143], v[16:23], v[174:181], v[140:143]
	v_mfma_f32_16x16x128_f8f6f4 v[136:139], v[24:31], v[174:181], v[136:139]
	v_mfma_f32_16x16x128_f8f6f4 v[124:127], v[16:23], v[182:189], v[124:127]
	v_mfma_f32_16x16x128_f8f6f4 v[120:123], v[24:31], v[182:189], v[120:123]
	v_mfma_f32_16x16x128_f8f6f4 v[108:111], v[16:23], v[216:223], v[108:111]
	v_mfma_f32_16x16x128_f8f6f4 v[104:107], v[24:31], v[216:223], v[104:107]
	s_setprio 0
	s_setprio 1
	v_mfma_f32_16x16x128_f8f6f4 v[148:151], v[8:15], v[166:173], v[148:151]
	v_mfma_f32_16x16x128_f8f6f4 v[144:147], v[0:7], v[166:173], v[144:147]
	v_mfma_f32_16x16x128_f8f6f4 v[132:135], v[8:15], v[174:181], v[132:135]
	v_mfma_f32_16x16x128_f8f6f4 v[128:131], v[0:7], v[174:181], v[128:131]
	v_mfma_f32_16x16x128_f8f6f4 v[116:119], v[8:15], v[182:189], v[116:119]
	v_mfma_f32_16x16x128_f8f6f4 v[112:115], v[0:7], v[182:189], v[112:115]
	v_mfma_f32_16x16x128_f8f6f4 v[100:103], v[8:15], v[216:223], v[100:103]
	v_mfma_f32_16x16x128_f8f6f4 v[96:99], v[0:7], v[216:223], v[96:99]
	s_setprio 0
	s_barrier
	s_cmp_gt_u32 s43, 24
	s_cselect_b64 vcc, -1, 0
	s_and_b64 s[44:45], vcc, exec
	s_cselect_b32 s44, 0xffffffe7, 3
	s_add_i32 s44, s44, s43
	s_ashr_i32 s45, s44, 31
	v_cndmask_b32_e32 v191, v161, v209, vcc
	v_cndmask_b32_e32 v190, v160, v208, vcc
	s_lshl_b64 s[44:45], s[44:45], 7
	v_lshl_add_u64 v[190:191], v[190:191], 0, s[44:45]
	s_add_i32 s46, s46, s66
	v_lshl_add_u64 v[224:225], v[190:191], 0, v[194:195]
	s_mov_b32 m0, s46
	ds_read_b128 v[166:169], v243 offset:49152
	ds_read_b128 v[170:173], v243 offset:50176
	ds_read_b128 v[174:177], v243 offset:51200
	ds_read_b128 v[178:181], v243 offset:52224
	ds_read_b128 v[182:185], v243 offset:53248
	ds_read_b128 v[186:189], v243 offset:54272
	ds_read_b128 v[216:219], v243 offset:55296
	ds_read_b128 v[220:223], v243 offset:56320
	global_load_lds_dwordx4 v[224:225], off
	v_lshl_add_u64 v[224:225], v[190:191], 0, v[198:199]
	s_add_i32 m0, s46, 0x2000
	v_lshl_add_u64 v[190:191], v[190:191], 0, s[0:1]
	s_add_i32 s46, s47, s66
	global_load_lds_dwordx4 v[224:225], off
	v_lshl_add_u64 v[224:225], v[190:191], 0, v[194:195]
	s_mov_b32 m0, s46
	v_lshl_add_u64 v[190:191], v[190:191], 0, v[198:199]
	global_load_lds_dwordx4 v[224:225], off
	s_add_i32 m0, s46, 0x2000
	s_and_b64 s[46:47], vcc, exec
	s_cselect_b32 s47, s62, s38
	s_cselect_b32 s46, s63, s39
	s_add_u32 s44, s47, s44
	s_addc_u32 s45, s46, s45
	global_load_lds_dwordx4 v[190:191], off
	s_mov_b32 m0, s78
	s_nop 0
	global_load_lds_dwordx4 v192, s[44:45]
	s_mov_b32 m0, s79
	s_nop 0
	global_load_lds_dwordx4 v196, s[44:45]
	s_waitcnt vmcnt(8)
	s_waitcnt lgkmcnt(0)
	s_barrier
	s_setprio 1
	s_waitcnt lgkmcnt(0)
	v_mfma_f32_16x16x128_f8f6f4 v[92:95], v[16:23], v[166:173], v[92:95]
	v_mfma_f32_16x16x128_f8f6f4 v[88:91], v[24:31], v[166:173], v[88:91]
	v_mfma_f32_16x16x128_f8f6f4 v[76:79], v[16:23], v[174:181], v[76:79]
	v_mfma_f32_16x16x128_f8f6f4 v[72:75], v[24:31], v[174:181], v[72:75]
	v_mfma_f32_16x16x128_f8f6f4 v[52:55], v[16:23], v[182:189], v[52:55]
	v_mfma_f32_16x16x128_f8f6f4 v[48:51], v[24:31], v[182:189], v[48:51]
	v_mfma_f32_16x16x128_f8f6f4 v[36:39], v[16:23], v[216:223], v[36:39]
	v_mfma_f32_16x16x128_f8f6f4 v[32:35], v[24:31], v[216:223], v[32:35]
	s_setprio 0
	s_setprio 1
	v_mfma_f32_16x16x128_f8f6f4 v[84:87], v[8:15], v[166:173], v[84:87]
	v_mfma_f32_16x16x128_f8f6f4 v[80:83], v[0:7], v[166:173], v[80:83]
	v_mfma_f32_16x16x128_f8f6f4 v[60:63], v[8:15], v[174:181], v[60:63]
	v_mfma_f32_16x16x128_f8f6f4 v[56:59], v[0:7], v[174:181], v[56:59]
	v_mfma_f32_16x16x128_f8f6f4 v[68:71], v[8:15], v[182:189], v[68:71]
	v_mfma_f32_16x16x128_f8f6f4 v[64:67], v[0:7], v[182:189], v[64:67]
	v_mfma_f32_16x16x128_f8f6f4 v[44:47], v[8:15], v[216:223], v[44:47]
	v_mfma_f32_16x16x128_f8f6f4 v[40:43], v[0:7], v[216:223], v[40:43]
	s_setprio 0
	s_barrier
	v_lshl_add_u64 v[162:163], v[162:163], 0, s[34:35]
	v_lshl_add_u64 v[164:165], v[164:165], 0, s[34:35]
	s_add_i32 s43, s43, 2
	s_and_b64 vcc, exec, s[40:41]
	s_cbranch_vccnz .LBB0_1263
	s_andn2_b64 vcc, exec, s[30:31]
	s_cbranch_vccnz .LBB0_1266
	s_barrier

.LBB0_1373:
	ds_read_b128 v[24:27], v217
	ds_read_b128 v[28:31], v217 offset:1024
	ds_read_b128 v[16:19], v217 offset:2048
	ds_read_b128 v[20:23], v217 offset:3072
	ds_read_b128 v[8:11], v221
	ds_read_b128 v[12:15], v221 offset:1024
	ds_read_b128 v[0:3], v221 offset:2048
	ds_read_b128 v[4:7], v221 offset:3072
	s_add_i32 m0, s70, 0xc000
	ds_read_b128 v[166:169], v225
	ds_read_b128 v[170:173], v225 offset:1024
	ds_read_b128 v[174:177], v225 offset:2048
	ds_read_b128 v[178:181], v225 offset:3072
	ds_read_b128 v[226:229], v225 offset:4096
	ds_read_b128 v[230:233], v225 offset:5120
	ds_read_b128 v[238:241], v225 offset:6144
	ds_read_b128 v[242:245], v225 offset:7168
	global_load_lds_dwordx4 v[162:163], off
	s_add_i32 m0, s70, 0xe000
	s_nop 0
	global_load_lds_dwordx4 v[164:165], off
	s_waitcnt vmcnt(8)
	s_waitcnt lgkmcnt(0)
	s_barrier
	s_setprio 1
	s_waitcnt lgkmcnt(0)
	v_mfma_f32_16x16x128_f8f6f4 v[156:159], v[24:31], v[166:173], v[156:159]
	v_mfma_f32_16x16x128_f8f6f4 v[152:155], v[16:23], v[166:173], v[152:155]
	v_mfma_f32_16x16x128_f8f6f4 v[140:143], v[24:31], v[174:181], v[140:143]
	v_mfma_f32_16x16x128_f8f6f4 v[136:139], v[16:23], v[174:181], v[136:139]
	v_mfma_f32_16x16x128_f8f6f4 v[124:127], v[24:31], v[226:233], v[124:127]
	v_mfma_f32_16x16x128_f8f6f4 v[120:123], v[16:23], v[226:233], v[120:123]
	v_mfma_f32_16x16x128_f8f6f4 v[108:111], v[24:31], v[238:245], v[108:111]
	v_mfma_f32_16x16x128_f8f6f4 v[104:107], v[16:23], v[238:245], v[104:107]
	s_setprio 0
	s_setprio 1
	v_mfma_f32_16x16x128_f8f6f4 v[148:151], v[8:15], v[166:173], v[148:151]
	v_mfma_f32_16x16x128_f8f6f4 v[144:147], v[0:7], v[166:173], v[144:147]
	v_mfma_f32_16x16x128_f8f6f4 v[132:135], v[8:15], v[174:181], v[132:135]
	v_mfma_f32_16x16x128_f8f6f4 v[128:131], v[0:7], v[174:181], v[128:131]
	v_mfma_f32_16x16x128_f8f6f4 v[116:119], v[8:15], v[226:233], v[116:119]
	v_mfma_f32_16x16x128_f8f6f4 v[112:115], v[0:7], v[226:233], v[112:115]
	v_mfma_f32_16x16x128_f8f6f4 v[100:103], v[8:15], v[238:245], v[100:103]
	v_mfma_f32_16x16x128_f8f6f4 v[96:99], v[0:7], v[238:245], v[96:99]
	s_setprio 0
	s_barrier
	s_cmp_gt_u32 s39, 25
	v_sub_co_u32_e64 v192, s[30:31], s39, 26
	s_cselect_b64 vcc, -1, 0
	v_add_u32_e32 v202, 28, v192
	v_cndmask_b32_e32 v208, v202, v192, vcc
	v_ashrrev_i32_e32 v209, 31, v208
	v_cndmask_b32_e32 v183, v161, v201, vcc
	v_cndmask_b32_e32 v182, v160, v200, vcc
	v_lshlrev_b64 v[208:209], 7, v[208:209]
	v_lshl_add_u64 v[182:183], v[182:183], 0, v[208:209]
	s_add_i32 s40, s6, s68
	v_lshl_add_u64 v[210:211], v[182:183], 0, v[186:187]
	s_mov_b32 m0, s40
	ds_read_b128 v[166:169], v225 offset:16384
	ds_read_b128 v[170:173], v225 offset:17408
	ds_read_b128 v[174:177], v225 offset:18432
	ds_read_b128 v[178:181], v225 offset:19456
	ds_read_b128 v[226:229], v225 offset:20480
	ds_read_b128 v[230:233], v225 offset:21504
	ds_read_b128 v[238:241], v225 offset:22528
	ds_read_b128 v[242:245], v225 offset:23552
	global_load_lds_dwordx4 v[210:211], off
	v_lshl_add_u64 v[210:211], v[182:183], 0, v[190:191]
	s_add_i32 m0, s40, 0x2000
	v_lshl_add_u64 v[182:183], v[182:183], 0, s[0:1]
	s_add_i32 s40, s79, s68
	global_load_lds_dwordx4 v[210:211], off
	v_lshl_add_u64 v[210:211], v[182:183], 0, v[186:187]
	s_mov_b32 m0, s40
	v_lshl_add_u64 v[182:183], v[182:183], 0, v[190:191]
	global_load_lds_dwordx4 v[210:211], off
	s_add_i32 m0, s40, 0x2000
	s_and_b64 s[40:41], vcc, exec
	s_cselect_b32 s41, s27, s29
	s_cselect_b32 s40, s26, s28
	global_load_lds_dwordx4 v[182:183], off
	v_lshl_add_u64 v[182:183], s[40:41], 0, v[208:209]
	v_lshl_add_u64 v[208:209], v[182:183], 0, v[184:185]
	s_mov_b32 m0, s70
	s_nop 0
	global_load_lds_dwordx4 v[208:209], off
	v_lshl_add_u64 v[208:209], v[182:183], 0, v[188:189]
	s_mov_b32 m0, s71
	s_nop 0
	global_load_lds_dwordx4 v[208:209], off
	s_waitcnt vmcnt(8)
	s_waitcnt lgkmcnt(0)
	s_barrier
	s_setprio 1
	s_waitcnt lgkmcnt(0)
	v_mfma_f32_16x16x128_f8f6f4 v[92:95], v[24:31], v[166:173], v[92:95]
	v_mfma_f32_16x16x128_f8f6f4 v[88:91], v[16:23], v[166:173], v[88:91]
	v_mfma_f32_16x16x128_f8f6f4 v[76:79], v[24:31], v[174:181], v[76:79]
	v_mfma_f32_16x16x128_f8f6f4 v[72:75], v[16:23], v[174:181], v[72:75]
	v_mfma_f32_16x16x128_f8f6f4 v[52:55], v[24:31], v[226:233], v[52:55]
	v_mfma_f32_16x16x128_f8f6f4 v[48:51], v[16:23], v[226:233], v[48:51]
	v_mfma_f32_16x16x128_f8f6f4 v[36:39], v[24:31], v[238:245], v[36:39]
	v_mfma_f32_16x16x128_f8f6f4 v[32:35], v[16:23], v[238:245], v[32:35]
	s_setprio 0
	s_setprio 1
	v_mfma_f32_16x16x128_f8f6f4 v[84:87], v[8:15], v[166:173], v[84:87]
	v_mfma_f32_16x16x128_f8f6f4 v[80:83], v[0:7], v[166:173], v[80:83]
	v_mfma_f32_16x16x128_f8f6f4 v[60:63], v[8:15], v[174:181], v[60:63]
	v_mfma_f32_16x16x128_f8f6f4 v[56:59], v[0:7], v[174:181], v[56:59]
	v_mfma_f32_16x16x128_f8f6f4 v[68:71], v[8:15], v[226:233], v[68:71]
	v_mfma_f32_16x16x128_f8f6f4 v[64:67], v[0:7], v[226:233], v[64:67]
	v_mfma_f32_16x16x128_f8f6f4 v[44:47], v[8:15], v[238:245], v[44:47]
	v_mfma_f32_16x16x128_f8f6f4 v[40:43], v[0:7], v[238:245], v[40:43]
	s_setprio 0
	s_barrier
	s_add_i32 s42, 0, 0x18000
	s_add_i32 s43, 0, 0x1c000
	v_add_u32_e32 v0, s42, v207
	v_add_u32_e32 v4, s43, v207
	ds_read_b128 v[16:19], v0
	ds_read_b128 v[20:23], v0 offset:1024
	ds_read_b128 v[24:27], v0 offset:2048
	ds_read_b128 v[28:31], v0 offset:3072
	ds_read_b128 v[8:11], v4
	ds_read_b128 v[12:15], v4 offset:1024
	ds_read_b128 v[0:3], v4 offset:2048
	ds_read_b128 v[4:7], v4 offset:3072
	v_lshl_add_u64 v[182:183], v[182:183], 0, s[0:1]
	s_mov_b32 m0, s77
	v_lshl_add_u64 v[208:209], v[182:183], 0, v[184:185]
	ds_read_b128 v[166:169], v225 offset:32768
	ds_read_b128 v[170:173], v225 offset:33792
	ds_read_b128 v[174:177], v225 offset:34816
	ds_read_b128 v[178:181], v225 offset:35840
	ds_read_b128 v[226:229], v225 offset:36864
	ds_read_b128 v[230:233], v225 offset:37888
	ds_read_b128 v[238:241], v225 offset:38912
	ds_read_b128 v[242:245], v225 offset:39936
	global_load_lds_dwordx4 v[208:209], off
	v_lshl_add_u64 v[182:183], v[182:183], 0, v[188:189]
	s_mov_b32 m0, s78
	s_nop 0
	global_load_lds_dwordx4 v[182:183], off
	s_waitcnt vmcnt(8)
	s_waitcnt lgkmcnt(0)
	s_barrier
	s_setprio 1
	s_waitcnt lgkmcnt(0)
	v_mfma_f32_16x16x128_f8f6f4 v[156:159], v[16:23], v[166:173], v[156:159]
	v_mfma_f32_16x16x128_f8f6f4 v[152:155], v[24:31], v[166:173], v[152:155]
	v_mfma_f32_16x16x128_f8f6f4 v[140:143], v[16:23], v[174:181], v[140:143]
	v_mfma_f32_16x16x128_f8f6f4 v[136:139], v[24:31], v[174:181], v[136:139]
	v_mfma_f32_16x16x128_f8f6f4 v[124:127], v[16:23], v[226:233], v[124:127]
	v_mfma_f32_16x16x128_f8f6f4 v[120:123], v[24:31], v[226:233], v[120:123]
	v_mfma_f32_16x16x128_f8f6f4 v[108:111], v[16:23], v[238:245], v[108:111]
	v_mfma_f32_16x16x128_f8f6f4 v[104:107], v[24:31], v[238:245], v[104:107]
	s_setprio 0
	s_setprio 1
	v_mfma_f32_16x16x128_f8f6f4 v[148:151], v[8:15], v[166:173], v[148:151]
	v_mfma_f32_16x16x128_f8f6f4 v[144:147], v[0:7], v[166:173], v[144:147]
	v_mfma_f32_16x16x128_f8f6f4 v[132:135], v[8:15], v[174:181], v[132:135]
	v_mfma_f32_16x16x128_f8f6f4 v[128:131], v[0:7], v[174:181], v[128:131]
	v_mfma_f32_16x16x128_f8f6f4 v[116:119], v[8:15], v[226:233], v[116:119]
	v_mfma_f32_16x16x128_f8f6f4 v[112:115], v[0:7], v[226:233], v[112:115]
	v_mfma_f32_16x16x128_f8f6f4 v[100:103], v[8:15], v[238:245], v[100:103]
	v_mfma_f32_16x16x128_f8f6f4 v[96:99], v[0:7], v[238:245], v[96:99]
	s_setprio 0
	s_barrier
	s_cmp_gt_u32 s39, 24
	s_cselect_b64 vcc, -1, 0
	s_and_b64 s[40:41], vcc, exec
	s_cselect_b32 s40, 0xffffffe7, 3
	s_add_i32 s40, s40, s39
	s_ashr_i32 s41, s40, 31
	v_cndmask_b32_e32 v183, v161, v201, vcc
	v_cndmask_b32_e32 v182, v160, v200, vcc
	s_lshl_b64 s[40:41], s[40:41], 7
	v_lshl_add_u64 v[182:183], v[182:183], 0, s[40:41]
	s_add_i32 s42, s42, s68
	v_lshl_add_u64 v[208:209], v[182:183], 0, v[186:187]
	s_mov_b32 m0, s42
	ds_read_b128 v[166:169], v225 offset:49152
	ds_read_b128 v[170:173], v225 offset:50176
	ds_read_b128 v[174:177], v225 offset:51200
	ds_read_b128 v[178:181], v225 offset:52224
	ds_read_b128 v[226:229], v225 offset:53248
	ds_read_b128 v[230:233], v225 offset:54272
	ds_read_b128 v[238:241], v225 offset:55296
	ds_read_b128 v[242:245], v225 offset:56320
	global_load_lds_dwordx4 v[208:209], off
	v_lshl_add_u64 v[208:209], v[182:183], 0, v[190:191]
	s_add_i32 m0, s42, 0x2000
	v_lshl_add_u64 v[182:183], v[182:183], 0, s[0:1]
	s_add_i32 s42, s43, s68
	global_load_lds_dwordx4 v[208:209], off
	v_lshl_add_u64 v[208:209], v[182:183], 0, v[186:187]
	s_mov_b32 m0, s42
	v_lshl_add_u64 v[182:183], v[182:183], 0, v[190:191]
	global_load_lds_dwordx4 v[208:209], off
	s_add_i32 m0, s42, 0x2000
	s_and_b64 s[42:43], vcc, exec
	s_cselect_b32 s43, s26, s28
	s_cselect_b32 s42, s27, s29
	s_add_u32 s40, s43, s40
	s_addc_u32 s41, s42, s41
	global_load_lds_dwordx4 v[182:183], off
	s_mov_b32 m0, s54
	s_nop 0
	global_load_lds_dwordx4 v184, s[40:41]
	s_mov_b32 m0, s55
	s_nop 0
	global_load_lds_dwordx4 v188, s[40:41]
	s_waitcnt vmcnt(8)
	s_waitcnt lgkmcnt(0)
	s_barrier
	s_setprio 1
	s_waitcnt lgkmcnt(0)
	v_mfma_f32_16x16x128_f8f6f4 v[92:95], v[16:23], v[166:173], v[92:95]
	v_mfma_f32_16x16x128_f8f6f4 v[88:91], v[24:31], v[166:173], v[88:91]
	v_mfma_f32_16x16x128_f8f6f4 v[76:79], v[16:23], v[174:181], v[76:79]
	v_mfma_f32_16x16x128_f8f6f4 v[72:75], v[24:31], v[174:181], v[72:75]
	v_mfma_f32_16x16x128_f8f6f4 v[52:55], v[16:23], v[226:233], v[52:55]
	v_mfma_f32_16x16x128_f8f6f4 v[48:51], v[24:31], v[226:233], v[48:51]
	v_mfma_f32_16x16x128_f8f6f4 v[36:39], v[16:23], v[238:245], v[36:39]
	v_mfma_f32_16x16x128_f8f6f4 v[32:35], v[24:31], v[238:245], v[32:35]
	s_setprio 0
	s_setprio 1
	v_mfma_f32_16x16x128_f8f6f4 v[84:87], v[8:15], v[166:173], v[84:87]
	v_mfma_f32_16x16x128_f8f6f4 v[80:83], v[0:7], v[166:173], v[80:83]
	v_mfma_f32_16x16x128_f8f6f4 v[60:63], v[8:15], v[174:181], v[60:63]
	v_mfma_f32_16x16x128_f8f6f4 v[56:59], v[0:7], v[174:181], v[56:59]
	v_mfma_f32_16x16x128_f8f6f4 v[68:71], v[8:15], v[226:233], v[68:71]
	v_mfma_f32_16x16x128_f8f6f4 v[64:67], v[0:7], v[226:233], v[64:67]
	v_mfma_f32_16x16x128_f8f6f4 v[44:47], v[8:15], v[238:245], v[44:47]
	v_mfma_f32_16x16x128_f8f6f4 v[40:43], v[0:7], v[238:245], v[40:43]
	s_setprio 0
	s_barrier
	v_lshl_add_u64 v[162:163], v[162:163], 0, s[24:25]
	v_lshl_add_u64 v[164:165], v[164:165], 0, s[24:25]
	s_add_i32 s39, s39, 2
	s_and_b64 vcc, exec, s[30:31]
	s_cbranch_vccnz .LBB0_1373
	s_andn2_b64 vcc, exec, s[22:23]
	s_cbranch_vccnz .LBB0_1376
	s_barrier
